# speedup vs baseline: 1.0369x; 1.0214x over previous
_Z6k_mainPKDF16_PKfS2_S2_PKmPjPfS6_:
	s_load_dwordx8 s[52:59], s[0:1], 0x0
	v_and_b32_e32 v5, 63, v0
	v_lshlrev_b32_e32 v1, 4, v5
	s_and_b32 s4, s2, 7
	v_lshlrev_b32_e32 v10, 2, v0
	s_waitcnt lgkmcnt(0)
	global_load_dwordx4 v[6:9], v1, s[58:59]
	v_mbcnt_lo_u32_b32 v1, -1, 0
	v_mbcnt_hi_u32_b32 v132, -1, v1
	v_lshl_or_b32 v1, s4, 12, v10
	global_load_dword v55, v1, s[56:57]
	global_load_dword v56, v1, s[56:57] offset:1024
	global_load_dword v63, v1, s[56:57] offset:2048
	global_load_dword v64, v1, s[56:57] offset:3072
	v_readfirstlane_b32 s28, v0
	s_lshl_b32 s3, s2, 5
	s_load_dwordx8 s[20:27], s[0:1], 0x20
	s_and_b32 s0, s28, 0xffffffc0
	s_and_b32 s1, s3, 0x7fffff00
	s_add_i32 s0, s0, s1
	v_and_b32_e32 v4, 31, v0
	s_lshl_b32 s29, s4, 6
	s_lshl_b32 s1, s0, 4
	v_or_b32_e32 v42, s0, v4
	s_or_b32 s0, s1, s29
	s_ashr_i32 s1, s0, 31
	s_lshl_b64 s[0:1], s[0:1], 6
	s_waitcnt lgkmcnt(0)
	s_add_u32 s0, s20, s0
	s_addc_u32 s1, s21, s1
	s_lshl_b32 s31, s4, 19
	s_add_u32 s4, s52, s31
	v_mov_b32_e32 v3, 0
	v_lshlrev_b32_e32 v2, 4, v0
	s_addc_u32 s5, s53, 0
	s_movk_i32 s8, 0x2000
	v_lshl_add_u64 v[46:47], s[4:5], 0, v[2:3]
	v_add_co_u32_e32 v44, vcc, s8, v46
	s_movk_i32 s9, 0x4000
	s_nop 0
	v_addc_co_u32_e32 v45, vcc, 0, v47, vcc
	v_add_co_u32_e32 v48, vcc, s9, v46
	s_movk_i32 s10, 0x6000
	s_nop 0
	v_addc_co_u32_e32 v49, vcc, 0, v47, vcc
	v_lshlrev_b32_e32 v11, 10, v0
	v_add_co_u32_e32 v50, vcc, s10, v46
	s_mov_b32 s7, 0x8000
	v_and_b32_e32 v10, 0x8000, v11
	v_and_b32_e32 v11, 64, v132
	v_addc_co_u32_e32 v51, vcc, 0, v47, vcc
	v_lshl_or_b32 v61, v4, 7, v10
	v_add_u32_e32 v62, 64, v11
	global_load_dwordx4 v[10:13], v2, s[4:5]
	v_add_co_u32_e32 v52, vcc, s7, v46
	v_xor_b32_e32 v43, 32, v132
	s_nop 0
	v_addc_co_u32_e32 v53, vcc, 0, v47, vcc
	global_load_dwordx4 v[14:17], v[44:45], off offset:-4096
	global_load_dwordx4 v[18:21], v[44:45], off
	global_load_dwordx4 v[22:25], v[48:49], off offset:-4096
	global_load_dwordx4 v[26:29], v[48:49], off
	global_load_dwordx4 v[30:33], v[50:51], off offset:-4096
	global_load_dwordx4 v[34:37], v[50:51], off
	global_load_dwordx4 v[38:41], v[52:53], off offset:-4096
	v_mov_b32_e32 v220, v42
	v_mov_b32_e32 v221, 0
	s_mov_b64 s[94:95], 0x9000
	v_lshl_add_u64 v[222:223], v[220:221], 2, s[54:55]
	v_lshl_add_u64 v[208:209], s[94:95], 0, v[46:47]
	s_mov_b64 s[94:95], 0xb000
	global_load_dword v216, v[222:223], off
	global_load_dword v217, v[222:223], off offset:128
	global_load_dword v218, v61, s[0:1]
	v_lshl_add_u64 v[210:211], s[94:95], 0, v[46:47]
	s_mov_b64 s[94:95], 0xd000
	global_load_dwordx4 v[176:179], v[208:209], off offset:-4096
	global_load_dwordx4 v[180:183], v[208:209], off
	v_lshl_add_u64 v[212:213], s[94:95], 0, v[46:47]
	s_mov_b64 s[94:95], 0xf000
	global_load_dwordx4 v[184:187], v[210:211], off offset:-4096
	global_load_dwordx4 v[188:191], v[210:211], off
	v_lshl_add_u64 v[214:215], s[94:95], 0, v[46:47]
	global_load_dwordx4 v[192:195], v[212:213], off offset:-4096
	global_load_dwordx4 v[196:199], v[212:213], off
	global_load_dwordx4 v[200:203], v[214:215], off offset:-4096
	global_load_dwordx4 v[204:207], v[214:215], off
	v_cmp_lt_i32_e32 vcc, v43, v62
	s_mov_b32 s6, 0x46000000
	v_lshlrev_b32_e32 v54, 1, v0
	v_or_b32_e32 v57, 0x1b000, v54
	v_or_b32_e32 v58, 0x1b800, v54
	v_or_b32_e32 v59, 0x1b200, v54
	v_or_b32_e32 v60, 0x1ba00, v54
	s_movk_i32 s34, 0x90
	s_mov_b32 s4, 0xf000
	s_mov_b32 s30, 0
	s_mov_b32 s7, 0x3e4ccccd
	s_waitcnt vmcnt(23)
	v_max_f32_e32 v1, v9, v9
	v_max_f32_e32 v8, v8, v8
	v_max_f32_e32 v1, v8, v1
	v_max3_f32 v1, v6, v7, v1
	v_cndmask_b32_e32 v7, v132, v43, vcc
	v_lshlrev_b32_e32 v133, 2, v7
	v_mov_b32_dpp v6, v1 quad_perm:[1,0,3,2] row_mask:0xf bank_mask:0xf bound_ctrl:1
	v_max_f32_e32 v6, v6, v6
	v_max_f32_e32 v1, v1, v6
	v_ashrrev_i32_e32 v43, 31, v42
	v_lshl_add_u64 v[8:9], v[42:43], 2, s[54:55]
	v_mov_b32_dpp v6, v1 quad_perm:[2,3,0,1] row_mask:0xf bank_mask:0xf bound_ctrl:1
	v_max_f32_e32 v6, v6, v6
	v_max_f32_e32 v1, v1, v6
	s_nop 1
	v_mov_b32_dpp v6, v1 row_half_mirror row_mask:0xf bank_mask:0xf bound_ctrl:1
	v_max_f32_e32 v6, v6, v6
	v_max_f32_e32 v1, v1, v6
	s_nop 1
	v_mov_b32_dpp v6, v1 row_mirror row_mask:0xf bank_mask:0xf bound_ctrl:1
	v_max_f32_e32 v6, v6, v6
	v_max_f32_e32 v1, v1, v6
	ds_swizzle_b32 v6, v1 offset:swizzle(SWAP,16)
	s_waitcnt lgkmcnt(0)
	v_max_f32_e32 v6, v6, v6
	v_max_f32_e32 v7, v1, v6
	ds_bpermute_b32 v44, v133, v7
	s_waitcnt lgkmcnt(0)
	v_max_f32_e32 v8, v44, v44
	v_max_f32_e32 v7, v7, v8
	s_waitcnt vmcnt(22)
	v_sub_f32_e32 v8, v55, v7
	s_waitcnt vmcnt(21)
	v_sub_f32_e32 v9, v56, v7
	v_mul_f32_e32 v42, 0x3fb8aa3b, v8
	v_mul_f32_e32 v8, 0x3e4ccccd, v8
	v_mul_f32_e32 v43, 0x3fb8aa3b, v9
	v_mul_f32_e32 v9, 0x3e4ccccd, v9
	v_mul_f32_e32 v8, 0x3fb8aa3b, v8
	v_mul_f32_e32 v9, 0x3fb8aa3b, v9
	v_exp_f32_e32 v8, v8
	v_exp_f32_e32 v42, v42
	v_exp_f32_e32 v9, v9
	v_exp_f32_e32 v43, v43
	v_cvt_f16_f32_e32 v8, v8
	v_fma_mixlo_f16 v42, v42, s6, 0
	v_cvt_f16_f32_e32 v9, v9
	v_fma_mixlo_f16 v43, v43, s6, 0
	ds_write_b16 v57, v42
	ds_write_b16 v59, v43
	ds_write_b16 v58, v8
	ds_write_b16 v60, v9
	s_waitcnt vmcnt(20)
	v_sub_f32_e32 v8, v63, v7
	v_mul_f32_e32 v9, 0x3fb8aa3b, v8
	v_exp_f32_e32 v9, v9
	v_mul_f32_e32 v8, 0x3e4ccccd, v8
	v_or_b32_e32 v42, 0x1b400, v54
	v_mul_f32_e32 v8, 0x3fb8aa3b, v8
	v_fma_mixlo_f16 v9, v9, s6, 0
	ds_write_b16 v42, v9
	s_waitcnt vmcnt(19)
	v_sub_f32_e32 v9, v64, v7
	v_exp_f32_e32 v8, v8
	v_mul_f32_e32 v42, 0x3fb8aa3b, v9
	v_mul_f32_e32 v9, 0x3e4ccccd, v9
	v_mul_f32_e32 v9, 0x3fb8aa3b, v9
	v_exp_f32_e32 v9, v9
	v_cvt_f16_f32_e32 v8, v8
	v_exp_f32_e32 v42, v42
	v_or_b32_e32 v43, 0x1bc00, v54
	v_cvt_f16_f32_e32 v9, v9
	ds_write_b16 v43, v8
	v_fma_mixlo_f16 v8, v42, s6, 0
	v_or_b32_e32 v42, 0x1b600, v54
	ds_write_b16 v42, v8
	v_or_b32_e32 v8, 0x1be00, v54
	ds_write_b16 v8, v9
	v_lshrrev_b32_e32 v8, 3, v0
	v_and_b32_e32 v9, 0x70, v2
	v_lshrrev_b32_e32 v144, 4, v0
	v_and_b32_e32 v144, 7, v144
	v_lshlrev_b32_e32 v144, 4, v144
	v_xor_b32_e32 v9, v9, v144
	v_lshl_add_u32 v144, v8, 7, v9
	v_add_co_u32_e32 v8, vcc, s4, v46
	s_mov_b32 s4, 0xa000
	s_nop 0
	v_addc_co_u32_e32 v9, vcc, 0, v47, vcc
	s_waitcnt vmcnt(18)
	ds_write_b128 v144, v[10:13]
	s_waitcnt vmcnt(17)
	ds_write_b128 v144, v[14:17] offset:4096
	s_waitcnt vmcnt(16)
	ds_write_b128 v144, v[18:21] offset:8192
	s_waitcnt vmcnt(15)
	ds_write_b128 v144, v[22:25] offset:12288
	s_waitcnt vmcnt(14)
	ds_write_b128 v144, v[26:29] offset:16384
	s_waitcnt vmcnt(13)
	ds_write_b128 v144, v[30:33] offset:20480
	s_waitcnt vmcnt(12)
	ds_write_b128 v144, v[34:37] offset:24576
	v_add_co_u32_e32 v20, vcc, s4, v46
	s_mov_b32 s4, 0xc000
	s_nop 0
	v_addc_co_u32_e32 v21, vcc, 0, v47, vcc
	v_add_co_u32_e32 v28, vcc, s4, v46
	s_mov_b32 s4, 0xe000
	s_nop 0
	v_addc_co_u32_e32 v29, vcc, 0, v47, vcc
	v_add_co_u32_e32 v36, vcc, s4, v46
	s_waitcnt vmcnt(11)
	ds_write_b128 v144, v[38:41] offset:28672
	v_addc_co_u32_e32 v37, vcc, 0, v47, vcc
	s_nop 0
	s_nop 0
	v_mov_b32_e32 v36, v3
	v_mov_b32_e32 v37, v3
	v_mov_b32_e32 v38, v3
	v_mov_b32_e32 v39, v3
	s_mov_b32 s4, 0x9e3779b9
	s_waitcnt vmcnt(8)
	v_cmp_eq_u32_e32 vcc, s4, v218
	v_mfma_f32_32x32x16_f16 a[0:15], v[36:39], v[36:39], 0
	v_add_u32_e32 v40, 0x10000, v144
	v_mfma_f32_32x32x16_f16 a[16:31], v[36:39], v[36:39], 0
	s_nop 0
	v_mfma_f32_32x32x16_f16 a[32:47], v[36:39], v[36:39], 0
	s_nop 0
	v_mfma_f32_32x32x16_f16 a[48:63], v[36:39], v[36:39], 0
	s_nop 0
	v_mfma_f32_32x32x16_f16 a[64:79], v[36:39], v[36:39], 0
	s_nop 0
	v_mfma_f32_32x32x16_f16 a[112:127], v[36:39], v[36:39], 0
	s_nop 0
	v_mfma_f32_32x32x16_f16 a[128:143], v[36:39], v[36:39], 0
	s_nop 0
	v_mfma_f32_32x32x16_f16 a[80:95], v[36:39], v[36:39], 0
	s_nop 0
	v_mfma_f32_32x32x16_f16 a[240:255], v[36:39], v[36:39], 0
	s_nop 0
	v_mfma_f32_32x32x16_f16 a[224:239], v[36:39], v[36:39], 0
	s_nop 0
	v_mfma_f32_32x32x16_f16 a[208:223], v[36:39], v[36:39], 0
	s_nop 0
	v_mfma_f32_32x32x16_f16 a[192:207], v[36:39], v[36:39], 0
	s_nop 0
	v_mfma_f32_32x32x16_f16 a[176:191], v[36:39], v[36:39], 0
	s_nop 0
	v_mfma_f32_32x32x16_f16 a[160:175], v[36:39], v[36:39], 0
	s_nop 0
	v_mfma_f32_32x32x16_f16 a[144:159], v[36:39], v[36:39], 0
	s_waitcnt vmcnt(7)
	ds_write_b128 v144, v[176:179] offset:36864
	s_waitcnt vmcnt(6)
	ds_write_b128 v144, v[180:183] offset:40960
	s_waitcnt vmcnt(5)
	ds_write_b128 v144, v[184:187] offset:45056
	s_waitcnt vmcnt(4)
	ds_write_b128 v144, v[188:191] offset:49152
	s_waitcnt vmcnt(3)
	ds_write_b128 v144, v[192:195] offset:53248
	s_waitcnt vmcnt(2)
	ds_write_b128 v144, v[196:199] offset:57344
	s_waitcnt vmcnt(1)
	ds_write_b128 v144, v[200:203] offset:61440
	s_waitcnt vmcnt(0)
	ds_write_b128 v40, v[204:207]
	v_mfma_f32_32x32x16_f16 a[96:111], v[36:39], v[36:39], 0
	s_and_saveexec_b64 s[4:5], vcc
	s_cbranch_execz .LBB1_2
	s_nop 0
.LBB1_2:
	s_or_b64 exec, exec, s[4:5]
	v_add_f32_e32 v1, v7, v216
	v_max_f32_e32 v8, 0, v1
	v_sub_f32_e32 v9, v1, v8
	v_fma_f32 v1, v1, s7, -v8
	v_mul_f32_e32 v1, 0x3fb8aa3b, v1
	v_mul_f32_e32 v8, 0xbfb8aa3b, v8
	v_exp_f32_e32 v1, v1
	v_exp_f32_e32 v8, v8
	v_add_f32_e32 v6, v7, v217
	v_max_f32_e32 v7, 0, v6
	v_mul_f32_e32 v10, 0x46000000, v1
	v_fma_mixlo_f16 v15, v1, s6, 0
	v_mul_f32_e32 v1, 0x46000000, v8
	v_sub_f32_e32 v8, v6, v7
	v_fma_f32 v6, v6, s7, -v7
	v_mul_f32_e32 v9, 0x3fb8aa3b, v9
	v_mul_f32_e32 v6, 0x3fb8aa3b, v6
	v_mul_f32_e32 v7, 0xbfb8aa3b, v7
	v_exp_f32_e32 v9, v9
	v_exp_f32_e32 v6, v6
	v_exp_f32_e32 v7, v7
	v_mul_f32_e32 v8, 0x3fb8aa3b, v8
	v_lshrrev_b32_e32 v5, 1, v5
	v_exp_f32_e32 v16, v8
	v_and_b32_e32 v5, 16, v5
	v_or_b32_e32 v142, 0x1b000, v5
	v_cvt_f16_f32_e32 v14, v9
	v_cvt_pk_f16_f32 v136, v9, v9
	v_cvt_pk_f16_f32 v137, v10, v10
	v_mul_f32_e32 v18, 0x46000000, v6
	v_fma_mixlo_f16 v22, v6, s6, 0
	v_mul_f32_e32 v19, 0x46000000, v7
	s_waitcnt lgkmcnt(0)
	s_barrier
	v_or_b32_e32 v143, 0x1b800, v5
	ds_read_b128 v[6:9], v142
	ds_read_b128 v[10:13], v143
	v_cvt_f16_f32_e32 v17, v16
	s_load_dwordx16 s[4:19], s[0:1], 0x0
	v_cvt_pk_f16_f32 v140, v16, v16
	v_cvt_pk_f16_f32 v139, v18, v18
	s_waitcnt lgkmcnt(0)
	v_pk_mul_f16 v16, v6, v14 op_sel_hi:[1,0]
	v_pk_mul_f16 v18, v10, v15 op_sel_hi:[1,0]
	v_cvt_pk_f16_f32 v1, v1, v1
	v_pk_max_f16 v16, v16, v18
	v_pk_mul_f16 v6, v6, v17 op_sel_hi:[1,0]
	v_pk_mul_f16 v10, v10, v22 op_sel_hi:[1,0]
	s_mov_b32 s33, 0x7060100
	v_pk_max_f16 v6, v6, v10
	v_cndmask_b32_e64 v10, v1, v16, s[4:5]
	v_cndmask_b32_e64 v16, v1, v16, s[6:7]
	v_perm_b32 v18, v16, v10, s33
	v_pk_mul_f16 v10, v7, v14 op_sel_hi:[1,0]
	v_pk_mul_f16 v16, v11, v15 op_sel_hi:[1,0]
	v_cvt_pk_f16_f32 v138, v19, v19
	v_pk_max_f16 v10, v10, v16
	s_load_dwordx16 s[36:51], s[0:1], 0x8000
	v_cndmask_b32_e64 v16, v1, v10, s[8:9]
	v_cndmask_b32_e64 v10, v1, v10, s[10:11]
	v_perm_b32 v19, v10, v16, s33
	v_pk_mul_f16 v10, v8, v14 op_sel_hi:[1,0]
	v_pk_mul_f16 v16, v12, v15 op_sel_hi:[1,0]
	v_pk_mul_f16 v7, v7, v17 op_sel_hi:[1,0]
	v_pk_max_f16 v10, v10, v16
	v_pk_mul_f16 v11, v11, v22 op_sel_hi:[1,0]
	v_cndmask_b32_e64 v16, v1, v10, s[12:13]
	v_cndmask_b32_e64 v10, v1, v10, s[14:15]
	v_perm_b32 v20, v10, v16, s33
	v_pk_mul_f16 v10, v9, v14 op_sel_hi:[1,0]
	v_pk_mul_f16 v14, v13, v15 op_sel_hi:[1,0]
	v_pk_mul_f16 v8, v8, v17 op_sel_hi:[1,0]
	v_pk_max_f16 v10, v10, v14
	v_pk_mul_f16 v12, v12, v22 op_sel_hi:[1,0]
	v_cndmask_b32_e64 v14, v1, v10, s[16:17]
	v_cndmask_b32_e64 v10, v1, v10, s[18:19]
	v_perm_b32 v21, v10, v14, s33
	v_pk_add_f16 v10, v19, v18
	v_pk_add_f16 v14, v20, v21
	v_pk_mul_f16 v9, v9, v17 op_sel_hi:[1,0]
	v_pk_mul_f16 v13, v13, v22 op_sel_hi:[1,0]
	v_pk_add_f16 v10, v10, v14
	v_mov_b32_e32 v134, v3
	v_pk_max_f16 v7, v7, v11
	v_pk_max_f16 v8, v8, v12
	v_pk_max_f16 v9, v9, v13
	v_dot2c_f32_f16_e32 v134, 0x3c003c00, v10
	s_waitcnt lgkmcnt(0)
	v_cndmask_b32_e64 v10, v138, v6, s[36:37]
	v_cndmask_b32_e64 v6, v138, v6, s[38:39]
	v_cndmask_b32_e64 v11, v138, v7, s[40:41]
	v_cndmask_b32_e64 v7, v138, v7, s[42:43]
	v_cndmask_b32_e64 v12, v138, v8, s[44:45]
	v_cndmask_b32_e64 v8, v138, v8, s[46:47]
	v_cndmask_b32_e64 v13, v138, v9, s[48:49]
	v_cndmask_b32_e64 v9, v138, v9, s[50:51]
	v_perm_b32 v38, v6, v10, s33
	v_perm_b32 v39, v7, v11, s33
	v_perm_b32 v40, v8, v12, s33
	v_perm_b32 v41, v9, v13, s33
	v_pk_add_f16 v6, v39, v38
	v_pk_add_f16 v7, v40, v41
	v_mov_b32_e32 v135, v3
	v_pk_add_f16 v6, v6, v7
	v_lshrrev_b32_e32 v211, 1, v4
	v_and_b32_e32 v211, 7, v211
	v_lshlrev_b32_e32 v211, 4, v211
	v_lshlrev_b32_e32 v141, 7, v4
	v_or_b32_e32 v208, 32, v5
	v_or_b32_e32 v209, 64, v5
	v_or_b32_e32 v210, 0x60, v5
	v_xor_b32_e32 v208, v208, v211
	v_xor_b32_e32 v209, v209, v211
	v_xor_b32_e32 v210, v210, v211
	v_xor_b32_e32 v211, v5, v211
	v_add_u32_e32 v208, v208, v141
	v_add_u32_e32 v209, v209, v141
	v_add_u32_e32 v210, v210, v141
	v_add_u32_e32 v141, v211, v141
	v_dot2c_f32_f16_e32 v135, 0x3c003c00, v6
	v_or_b32_e32 v6, 0x1b020, v5
	s_load_dwordx16 s[36:51], s[0:1], 0x40
	s_load_dwordx16 s[4:19], s[0:1], 0x8040
	v_or_b32_e32 v7, 0x1b820, v5
	ds_read_b128 v[46:49], v6
	ds_read_b128 v[42:45], v7
	ds_read_b128 v[74:77], v141
	ds_read_b128 v[126:129], v141 offset:4096
	ds_read_b128 v[122:125], v141 offset:8192
	ds_read_b128 v[118:121], v141 offset:12288
	ds_read_b128 v[106:109], v141 offset:16384
	ds_read_b128 v[98:101], v141 offset:20480
	ds_read_b128 v[94:97], v141 offset:24576
	ds_read_b128 v[86:89], v141 offset:28672
	s_add_u32 s34, s52, s31
	s_addc_u32 s35, s53, 0
	s_add_u32 s94, s34, 0x10000
	s_addc_u32 s95, s35, 0
	v_mov_b32_e32 v164, v144
	v_add_u32_e32 v165, 0x1000, v144
	v_add_u32_e32 v166, 0x2000, v144
	v_add_u32_e32 v167, 0x3000, v144
	v_add_u32_e32 v168, 0x4000, v144
	v_add_u32_e32 v169, 0x5000, v144
	v_add_u32_e32 v170, 0x6000, v144
	v_add_u32_e32 v171, 0x7000, v144
	s_lshl_b32 s31, s2, 9
	s_lshl_b32 s28, s28, 4
	s_and_b32 s31, s31, 0xfffff000
	s_and_b32 s28, s28, 0xfffffc00
	s_mov_b32 s93, s28
	s_add_i32 s31, s31, s28
	s_or_b32 s28, s31, s29
	s_ashr_i32 s29, s28, 31
	v_lshl_add_u64 v[2:3], s[34:35], 0, v[2:3]
	s_mov_b64 s[34:35], 0x1700c
	s_lshl_b64 s[28:29], s[28:29], 6
	v_lshl_add_u64 v[130:131], v[2:3], 0, s[34:35]
	s_add_u32 s35, s20, s28
	v_or_b32_e32 v145, 0x1b040, v5
	s_movk_i32 s34, 0xf000
	s_addc_u32 s84, s21, s29
	s_mov_b64 s[20:21], 0
	s_movk_i32 s85, 0x9000
	s_movk_i32 s86, 0xa000
	s_movk_i32 s87, 0xb000
	s_movk_i32 s88, 0xc000
	s_movk_i32 s89, 0xd000
	s_movk_i32 s90, 0xe000
	s_mov_b64 s[28:29], 0x8000
.LBB1_3:
	s_waitcnt lgkmcnt(0)
	v_mfma_f32_32x32x16_f16 a[0:15], v[18:21], v[74:77], a[0:15]
	s_add_i32 s31, s30, 1
	s_cmp_lg_u32 s30, 2
	s_cselect_b32 s91, s31, 0
	s_mul_i32 s30, s30, 0x9000
	s_mul_i32 s92, s91, 0x9000
	v_add_u32_e32 v147, s30, v208
	v_add_u32_e32 v2, s30, v209
	v_add_u32_e32 v3, s30, v210
	v_add_u32_e32 v146, s92, v141
	s_add_u32 s30, s35, s20
	s_addc_u32 s31, s84, s21
	s_add_i32 s96, s92, 0x9000
	s_cmp_lg_u32 s91, 2
	s_cselect_b32 s96, s96, 0
	s_add_i32 s96, s96, s93
	s_mov_b32 m0, s96
	s_nop 0
	global_load_lds_dwordx4 v164, s[94:95]
	s_add_u32 m0, s96, 0x1000
	s_nop 0
	global_load_lds_dwordx4 v165, s[94:95]
	s_add_u32 m0, s96, 0x2000
	s_nop 0
	global_load_lds_dwordx4 v166, s[94:95]
	s_add_u32 m0, s96, 0x3000
	s_nop 0
	global_load_lds_dwordx4 v167, s[94:95]
	s_add_u32 m0, s96, 0x4000
	s_nop 0
	global_load_lds_dwordx4 v168, s[94:95]
	s_add_u32 m0, s96, 0x5000
	s_nop 0
	global_load_lds_dwordx4 v169, s[94:95]
	s_add_u32 m0, s96, 0x6000
	s_nop 0
	global_load_lds_dwordx4 v170, s[94:95]
	s_add_u32 m0, s96, 0x7000
	s_nop 0
	global_load_lds_dwordx4 v171, s[94:95]
	s_load_dwordx16 s[68:83], s[30:31], 0x80
	s_load_dwordx16 s[52:67], s[30:31], 0x8080
	ds_read_b128 v[90:93], v145
	ds_read_b128 v[82:85], v145 offset:2048
	v_mfma_f32_32x32x16_f16 a[240:255], v[38:41], v[74:77], a[240:255]
	ds_read_b128 v[50:53], v147
	v_pk_mul_f16 v148, v46, v136
	v_pk_mul_f16 v149, v42, v137
	v_pk_mul_f16 v150, v47, v136
	v_pk_mul_f16 v151, v43, v137
	v_mfma_f32_32x32x16_f16 a[16:31], v[18:21], v[126:129], a[16:31]
	ds_read_b128 v[54:57], v147 offset:4096
	v_pk_mul_f16 v152, v48, v136
	v_pk_mul_f16 v153, v44, v137
	v_pk_mul_f16 v154, v49, v136
	v_pk_mul_f16 v155, v45, v137
	v_mfma_f32_32x32x16_f16 a[224:239], v[38:41], v[126:129], a[224:239]
	ds_read_b128 v[58:61], v147 offset:8192
	v_pk_mul_f16 v156, v46, v140
	v_pk_mul_f16 v157, v42, v139
	v_pk_mul_f16 v158, v47, v140
	v_pk_mul_f16 v159, v43, v139
	v_mfma_f32_32x32x16_f16 a[32:47], v[18:21], v[122:125], a[32:47]
	ds_read_b128 v[62:65], v147 offset:12288
	v_pk_mul_f16 v160, v48, v140
	v_pk_mul_f16 v161, v44, v139
	v_pk_mul_f16 v162, v49, v140
	v_pk_mul_f16 v163, v45, v139
	v_mfma_f32_32x32x16_f16 a[208:223], v[38:41], v[122:125], a[208:223]
	ds_read_b128 v[66:69], v147 offset:16384
	v_pk_max_f16 v148, v148, v149
	v_pk_max_f16 v150, v150, v151
	v_pk_max_f16 v152, v152, v153
	v_pk_max_f16 v154, v154, v155
	v_mfma_f32_32x32x16_f16 a[48:63], v[18:21], v[118:121], a[48:63]
	ds_read_b128 v[70:73], v147 offset:20480
	v_pk_max_f16 v156, v156, v157
	v_pk_max_f16 v158, v158, v159
	v_pk_max_f16 v160, v160, v161
	v_pk_max_f16 v162, v162, v163
	v_mfma_f32_32x32x16_f16 a[192:207], v[38:41], v[118:121], a[192:207]
	ds_read_b128 v[78:81], v147 offset:24576
	v_cndmask_b32_e64 v114, v1, v148, s[36:37]
	s_mov_b64 vcc, s[38:39]
	v_cndmask_b32_sdwa v114, v1, v148, vcc dst_sel:WORD_1 dst_unused:UNUSED_PRESERVE src0_sel:WORD_1 src1_sel:WORD_1
	v_cndmask_b32_e64 v115, v1, v150, s[40:41]
	s_mov_b64 vcc, s[42:43]
	v_cndmask_b32_sdwa v115, v1, v150, vcc dst_sel:WORD_1 dst_unused:UNUSED_PRESERVE src0_sel:WORD_1 src1_sel:WORD_1
	v_mfma_f32_32x32x16_f16 a[64:79], v[18:21], v[106:109], a[64:79]
	ds_read_b128 v[102:105], v147 offset:28672
	v_cndmask_b32_e64 v116, v1, v152, s[44:45]
	s_mov_b64 vcc, s[46:47]
	v_cndmask_b32_sdwa v116, v1, v152, vcc dst_sel:WORD_1 dst_unused:UNUSED_PRESERVE src0_sel:WORD_1 src1_sel:WORD_1
	v_cndmask_b32_e64 v117, v1, v154, s[48:49]
	s_mov_b64 vcc, s[50:51]
	v_cndmask_b32_sdwa v117, v1, v154, vcc dst_sel:WORD_1 dst_unused:UNUSED_PRESERVE src0_sel:WORD_1 src1_sel:WORD_1
	v_mfma_f32_32x32x16_f16 a[176:191], v[38:41], v[106:109], a[176:191]
	v_cndmask_b32_e64 v110, v138, v156, s[4:5]
	s_mov_b64 vcc, s[6:7]
	v_cndmask_b32_sdwa v110, v138, v156, vcc dst_sel:WORD_1 dst_unused:UNUSED_PRESERVE src0_sel:WORD_1 src1_sel:WORD_1
	v_cndmask_b32_e64 v111, v138, v158, s[8:9]
	s_mov_b64 vcc, s[10:11]
	v_cndmask_b32_sdwa v111, v138, v158, vcc dst_sel:WORD_1 dst_unused:UNUSED_PRESERVE src0_sel:WORD_1 src1_sel:WORD_1
	v_mfma_f32_32x32x16_f16 a[112:127], v[18:21], v[98:101], a[112:127]
	v_cndmask_b32_e64 v112, v138, v160, s[12:13]
	s_mov_b64 vcc, s[14:15]
	v_cndmask_b32_sdwa v112, v138, v160, vcc dst_sel:WORD_1 dst_unused:UNUSED_PRESERVE src0_sel:WORD_1 src1_sel:WORD_1
	v_cndmask_b32_e64 v113, v138, v162, s[16:17]
	s_mov_b64 vcc, s[18:19]
	v_cndmask_b32_sdwa v113, v138, v162, vcc dst_sel:WORD_1 dst_unused:UNUSED_PRESERVE src0_sel:WORD_1 src1_sel:WORD_1
	v_mfma_f32_32x32x16_f16 a[160:175], v[38:41], v[98:101], a[160:175]
	v_pk_add_f16 v148, v115, v114
	v_pk_add_f16 v149, v116, v117
	v_mfma_f32_32x32x16_f16 a[128:143], v[18:21], v[94:97], a[128:143]
	v_pk_add_f16 v150, v111, v110
	v_pk_add_f16 v151, v112, v113
	v_mfma_f32_32x32x16_f16 a[144:159], v[38:41], v[94:97], a[144:159]
	v_pk_add_f16 v148, v148, v149
	v_pk_add_f16 v150, v150, v151
	v_mfma_f32_32x32x16_f16 a[80:95], v[18:21], v[86:89], a[80:95]
	v_dot2c_f32_f16_e32 v134, 0x3c003c00, v148
	v_dot2c_f32_f16_e32 v135, 0x3c003c00, v150
	v_mfma_f32_32x32x16_f16 a[96:111], v[38:41], v[86:89], a[96:111]
	s_waitcnt lgkmcnt(0)
	v_mfma_f32_32x32x16_f16 a[0:15], v[114:117], v[50:53], a[0:15]
	s_load_dwordx16 s[36:51], s[30:31], 0xc0
	s_load_dwordx16 s[4:19], s[30:31], 0x80c0
	ds_read_b128 v[46:49], v145 offset:32
	ds_read_b128 v[42:45], v145 offset:2080
	v_mfma_f32_32x32x16_f16 a[240:255], v[110:113], v[50:53], a[240:255]
	ds_read_b128 v[74:77], v2
	v_pk_mul_f16 v148, v90, v136
	v_pk_mul_f16 v149, v82, v137
	v_pk_mul_f16 v150, v91, v136
	v_pk_mul_f16 v151, v83, v137
	v_mfma_f32_32x32x16_f16 a[16:31], v[114:117], v[54:57], a[16:31]
	ds_read_b128 v[126:129], v2 offset:4096
	v_pk_mul_f16 v152, v92, v136
	v_pk_mul_f16 v153, v84, v137
	v_pk_mul_f16 v154, v93, v136
	v_pk_mul_f16 v155, v85, v137
	v_mfma_f32_32x32x16_f16 a[224:239], v[110:113], v[54:57], a[224:239]
	ds_read_b128 v[122:125], v2 offset:8192
	v_pk_mul_f16 v156, v90, v140
	v_pk_mul_f16 v157, v82, v139
	v_pk_mul_f16 v158, v91, v140
	v_pk_mul_f16 v159, v83, v139
	v_mfma_f32_32x32x16_f16 a[32:47], v[114:117], v[58:61], a[32:47]
	ds_read_b128 v[118:121], v2 offset:12288
	v_pk_mul_f16 v160, v92, v140
	v_pk_mul_f16 v161, v84, v139
	v_pk_mul_f16 v162, v93, v140
	v_pk_mul_f16 v163, v85, v139
	v_mfma_f32_32x32x16_f16 a[208:223], v[110:113], v[58:61], a[208:223]
	ds_read_b128 v[106:109], v2 offset:16384
	v_pk_max_f16 v148, v148, v149
	v_pk_max_f16 v150, v150, v151
	v_pk_max_f16 v152, v152, v153
	v_pk_max_f16 v154, v154, v155
	v_mfma_f32_32x32x16_f16 a[48:63], v[114:117], v[62:65], a[48:63]
	ds_read_b128 v[98:101], v2 offset:20480
	v_pk_max_f16 v156, v156, v157
	v_pk_max_f16 v158, v158, v159
	v_pk_max_f16 v160, v160, v161
	v_pk_max_f16 v162, v162, v163
	v_mfma_f32_32x32x16_f16 a[192:207], v[110:113], v[62:65], a[192:207]
	ds_read_b128 v[94:97], v2 offset:24576
	v_cndmask_b32_e64 v18, v1, v148, s[68:69]
	s_mov_b64 vcc, s[70:71]
	v_cndmask_b32_sdwa v18, v1, v148, vcc dst_sel:WORD_1 dst_unused:UNUSED_PRESERVE src0_sel:WORD_1 src1_sel:WORD_1
	v_cndmask_b32_e64 v19, v1, v150, s[72:73]
	s_mov_b64 vcc, s[74:75]
	v_cndmask_b32_sdwa v19, v1, v150, vcc dst_sel:WORD_1 dst_unused:UNUSED_PRESERVE src0_sel:WORD_1 src1_sel:WORD_1
	v_mfma_f32_32x32x16_f16 a[64:79], v[114:117], v[66:69], a[64:79]
	ds_read_b128 v[86:89], v2 offset:28672
	v_cndmask_b32_e64 v20, v1, v152, s[76:77]
	s_mov_b64 vcc, s[78:79]
	v_cndmask_b32_sdwa v20, v1, v152, vcc dst_sel:WORD_1 dst_unused:UNUSED_PRESERVE src0_sel:WORD_1 src1_sel:WORD_1
	v_cndmask_b32_e64 v21, v1, v154, s[80:81]
	s_mov_b64 vcc, s[82:83]
	v_cndmask_b32_sdwa v21, v1, v154, vcc dst_sel:WORD_1 dst_unused:UNUSED_PRESERVE src0_sel:WORD_1 src1_sel:WORD_1
	v_mfma_f32_32x32x16_f16 a[176:191], v[110:113], v[66:69], a[176:191]
	v_cndmask_b32_e64 v38, v138, v156, s[52:53]
	s_mov_b64 vcc, s[54:55]
	v_cndmask_b32_sdwa v38, v138, v156, vcc dst_sel:WORD_1 dst_unused:UNUSED_PRESERVE src0_sel:WORD_1 src1_sel:WORD_1
	v_cndmask_b32_e64 v39, v138, v158, s[56:57]
	s_mov_b64 vcc, s[58:59]
	v_cndmask_b32_sdwa v39, v138, v158, vcc dst_sel:WORD_1 dst_unused:UNUSED_PRESERVE src0_sel:WORD_1 src1_sel:WORD_1
	v_mfma_f32_32x32x16_f16 a[112:127], v[114:117], v[70:73], a[112:127]
	v_cndmask_b32_e64 v40, v138, v160, s[60:61]
	s_mov_b64 vcc, s[62:63]
	v_cndmask_b32_sdwa v40, v138, v160, vcc dst_sel:WORD_1 dst_unused:UNUSED_PRESERVE src0_sel:WORD_1 src1_sel:WORD_1
	v_cndmask_b32_e64 v41, v138, v162, s[64:65]
	s_mov_b64 vcc, s[66:67]
	v_cndmask_b32_sdwa v41, v138, v162, vcc dst_sel:WORD_1 dst_unused:UNUSED_PRESERVE src0_sel:WORD_1 src1_sel:WORD_1
	v_mfma_f32_32x32x16_f16 a[160:175], v[110:113], v[70:73], a[160:175]
	v_pk_add_f16 v148, v19, v18
	v_pk_add_f16 v149, v20, v21
	v_mfma_f32_32x32x16_f16 a[128:143], v[114:117], v[78:81], a[128:143]
	v_pk_add_f16 v150, v39, v38
	v_pk_add_f16 v151, v40, v41
	v_mfma_f32_32x32x16_f16 a[144:159], v[110:113], v[78:81], a[144:159]
	v_pk_add_f16 v148, v148, v149
	v_pk_add_f16 v150, v150, v151
	v_mfma_f32_32x32x16_f16 a[80:95], v[114:117], v[102:105], a[80:95]
	v_dot2c_f32_f16_e32 v134, 0x3c003c00, v148
	v_dot2c_f32_f16_e32 v135, 0x3c003c00, v150
	v_mfma_f32_32x32x16_f16 a[96:111], v[110:113], v[102:105], a[96:111]
	s_waitcnt lgkmcnt(0)
	v_mfma_f32_32x32x16_f16 a[0:15], v[18:21], v[74:77], a[0:15]
	s_load_dwordx16 s[68:83], s[30:31], 0x100
	s_load_dwordx16 s[52:67], s[30:31], 0x8100
	ds_read_b128 v[90:93], v145 offset:64
	ds_read_b128 v[82:85], v145 offset:2112
	v_mfma_f32_32x32x16_f16 a[240:255], v[38:41], v[74:77], a[240:255]
	ds_read_b128 v[50:53], v3
	v_pk_mul_f16 v148, v46, v136
	v_pk_mul_f16 v149, v42, v137
	v_pk_mul_f16 v150, v47, v136
	v_pk_mul_f16 v151, v43, v137
	v_mfma_f32_32x32x16_f16 a[16:31], v[18:21], v[126:129], a[16:31]
	ds_read_b128 v[54:57], v3 offset:4096
	v_pk_mul_f16 v152, v48, v136
	v_pk_mul_f16 v153, v44, v137
	v_pk_mul_f16 v154, v49, v136
	v_pk_mul_f16 v155, v45, v137
	v_mfma_f32_32x32x16_f16 a[224:239], v[38:41], v[126:129], a[224:239]
	ds_read_b128 v[58:61], v3 offset:8192
	v_pk_mul_f16 v156, v46, v140
	v_pk_mul_f16 v157, v42, v139
	v_pk_mul_f16 v158, v47, v140
	v_pk_mul_f16 v159, v43, v139
	v_mfma_f32_32x32x16_f16 a[32:47], v[18:21], v[122:125], a[32:47]
	ds_read_b128 v[62:65], v3 offset:12288
	v_pk_mul_f16 v160, v48, v140
	v_pk_mul_f16 v161, v44, v139
	v_pk_mul_f16 v162, v49, v140
	v_pk_mul_f16 v163, v45, v139
	v_mfma_f32_32x32x16_f16 a[208:223], v[38:41], v[122:125], a[208:223]
	ds_read_b128 v[66:69], v3 offset:16384
	v_pk_max_f16 v148, v148, v149
	v_pk_max_f16 v150, v150, v151
	v_pk_max_f16 v152, v152, v153
	v_pk_max_f16 v154, v154, v155
	v_mfma_f32_32x32x16_f16 a[48:63], v[18:21], v[118:121], a[48:63]
	ds_read_b128 v[70:73], v3 offset:20480
	v_pk_max_f16 v156, v156, v157
	v_pk_max_f16 v158, v158, v159
	v_pk_max_f16 v160, v160, v161
	v_pk_max_f16 v162, v162, v163
	v_mfma_f32_32x32x16_f16 a[192:207], v[38:41], v[118:121], a[192:207]
	ds_read_b128 v[78:81], v3 offset:24576
	v_cndmask_b32_e64 v114, v1, v148, s[36:37]
	s_mov_b64 vcc, s[38:39]
	v_cndmask_b32_sdwa v114, v1, v148, vcc dst_sel:WORD_1 dst_unused:UNUSED_PRESERVE src0_sel:WORD_1 src1_sel:WORD_1
	v_cndmask_b32_e64 v115, v1, v150, s[40:41]
	s_mov_b64 vcc, s[42:43]
	v_cndmask_b32_sdwa v115, v1, v150, vcc dst_sel:WORD_1 dst_unused:UNUSED_PRESERVE src0_sel:WORD_1 src1_sel:WORD_1
	v_mfma_f32_32x32x16_f16 a[64:79], v[18:21], v[106:109], a[64:79]
	ds_read_b128 v[102:105], v3 offset:28672
	v_cndmask_b32_e64 v116, v1, v152, s[44:45]
	s_mov_b64 vcc, s[46:47]
	v_cndmask_b32_sdwa v116, v1, v152, vcc dst_sel:WORD_1 dst_unused:UNUSED_PRESERVE src0_sel:WORD_1 src1_sel:WORD_1
	v_cndmask_b32_e64 v117, v1, v154, s[48:49]
	s_mov_b64 vcc, s[50:51]
	v_cndmask_b32_sdwa v117, v1, v154, vcc dst_sel:WORD_1 dst_unused:UNUSED_PRESERVE src0_sel:WORD_1 src1_sel:WORD_1
	v_mfma_f32_32x32x16_f16 a[176:191], v[38:41], v[106:109], a[176:191]
	v_cndmask_b32_e64 v110, v138, v156, s[4:5]
	s_mov_b64 vcc, s[6:7]
	v_cndmask_b32_sdwa v110, v138, v156, vcc dst_sel:WORD_1 dst_unused:UNUSED_PRESERVE src0_sel:WORD_1 src1_sel:WORD_1
	v_cndmask_b32_e64 v111, v138, v158, s[8:9]
	s_mov_b64 vcc, s[10:11]
	v_cndmask_b32_sdwa v111, v138, v158, vcc dst_sel:WORD_1 dst_unused:UNUSED_PRESERVE src0_sel:WORD_1 src1_sel:WORD_1
	v_mfma_f32_32x32x16_f16 a[112:127], v[18:21], v[98:101], a[112:127]
	v_cndmask_b32_e64 v112, v138, v160, s[12:13]
	s_mov_b64 vcc, s[14:15]
	v_cndmask_b32_sdwa v112, v138, v160, vcc dst_sel:WORD_1 dst_unused:UNUSED_PRESERVE src0_sel:WORD_1 src1_sel:WORD_1
	v_cndmask_b32_e64 v113, v138, v162, s[16:17]
	s_mov_b64 vcc, s[18:19]
	v_cndmask_b32_sdwa v113, v138, v162, vcc dst_sel:WORD_1 dst_unused:UNUSED_PRESERVE src0_sel:WORD_1 src1_sel:WORD_1
	v_mfma_f32_32x32x16_f16 a[160:175], v[38:41], v[98:101], a[160:175]
	v_pk_add_f16 v148, v115, v114
	v_pk_add_f16 v149, v116, v117
	v_mfma_f32_32x32x16_f16 a[128:143], v[18:21], v[94:97], a[128:143]
	v_pk_add_f16 v150, v111, v110
	v_pk_add_f16 v151, v112, v113
	v_mfma_f32_32x32x16_f16 a[144:159], v[38:41], v[94:97], a[144:159]
	v_pk_add_f16 v148, v148, v149
	v_pk_add_f16 v150, v150, v151
	v_mfma_f32_32x32x16_f16 a[80:95], v[18:21], v[86:89], a[80:95]
	v_dot2c_f32_f16_e32 v134, 0x3c003c00, v148
	v_dot2c_f32_f16_e32 v135, 0x3c003c00, v150
	v_mfma_f32_32x32x16_f16 a[96:111], v[38:41], v[86:89], a[96:111]
	s_waitcnt lgkmcnt(0)
	v_mfma_f32_32x32x16_f16 a[0:15], v[114:117], v[50:53], a[0:15]
	s_load_dwordx16 s[36:51], s[30:31], 0x140
	s_load_dwordx16 s[4:19], s[30:31], 0x8140
	ds_read_b128 v[46:49], v145 offset:96
	ds_read_b128 v[42:45], v145 offset:2144
	v_mfma_f32_32x32x16_f16 a[240:255], v[110:113], v[50:53], a[240:255]
	ds_read_b128 v[74:77], v146
	v_pk_mul_f16 v148, v90, v136
	v_pk_mul_f16 v149, v82, v137
	v_pk_mul_f16 v150, v91, v136
	v_pk_mul_f16 v151, v83, v137
	v_mfma_f32_32x32x16_f16 a[16:31], v[114:117], v[54:57], a[16:31]
	ds_read_b128 v[126:129], v146 offset:4096
	v_pk_mul_f16 v152, v92, v136
	v_pk_mul_f16 v153, v84, v137
	v_pk_mul_f16 v154, v93, v136
	v_pk_mul_f16 v155, v85, v137
	v_mfma_f32_32x32x16_f16 a[224:239], v[110:113], v[54:57], a[224:239]
	ds_read_b128 v[122:125], v146 offset:8192
	v_pk_mul_f16 v156, v90, v140
	v_pk_mul_f16 v157, v82, v139
	v_pk_mul_f16 v158, v91, v140
	v_pk_mul_f16 v159, v83, v139
	v_mfma_f32_32x32x16_f16 a[32:47], v[114:117], v[58:61], a[32:47]
	ds_read_b128 v[118:121], v146 offset:12288
	v_pk_mul_f16 v160, v92, v140
	v_pk_mul_f16 v161, v84, v139
	v_pk_mul_f16 v162, v93, v140
	v_pk_mul_f16 v163, v85, v139
	v_mfma_f32_32x32x16_f16 a[208:223], v[110:113], v[58:61], a[208:223]
	ds_read_b128 v[106:109], v146 offset:16384
	v_pk_max_f16 v148, v148, v149
	v_pk_max_f16 v150, v150, v151
	v_pk_max_f16 v152, v152, v153
	v_pk_max_f16 v154, v154, v155
	v_mfma_f32_32x32x16_f16 a[48:63], v[114:117], v[62:65], a[48:63]
	ds_read_b128 v[98:101], v146 offset:20480
	v_pk_max_f16 v156, v156, v157
	v_pk_max_f16 v158, v158, v159
	v_pk_max_f16 v160, v160, v161
	v_pk_max_f16 v162, v162, v163
	v_mfma_f32_32x32x16_f16 a[192:207], v[110:113], v[62:65], a[192:207]
	ds_read_b128 v[94:97], v146 offset:24576
	v_cndmask_b32_e64 v18, v1, v148, s[68:69]
	s_mov_b64 vcc, s[70:71]
	v_cndmask_b32_sdwa v18, v1, v148, vcc dst_sel:WORD_1 dst_unused:UNUSED_PRESERVE src0_sel:WORD_1 src1_sel:WORD_1
	v_cndmask_b32_e64 v19, v1, v150, s[72:73]
	s_mov_b64 vcc, s[74:75]
	v_cndmask_b32_sdwa v19, v1, v150, vcc dst_sel:WORD_1 dst_unused:UNUSED_PRESERVE src0_sel:WORD_1 src1_sel:WORD_1
	v_mfma_f32_32x32x16_f16 a[64:79], v[114:117], v[66:69], a[64:79]
	ds_read_b128 v[86:89], v146 offset:28672
	v_cndmask_b32_e64 v20, v1, v152, s[76:77]
	s_mov_b64 vcc, s[78:79]
	v_cndmask_b32_sdwa v20, v1, v152, vcc dst_sel:WORD_1 dst_unused:UNUSED_PRESERVE src0_sel:WORD_1 src1_sel:WORD_1
	v_cndmask_b32_e64 v21, v1, v154, s[80:81]
	s_mov_b64 vcc, s[82:83]
	v_cndmask_b32_sdwa v21, v1, v154, vcc dst_sel:WORD_1 dst_unused:UNUSED_PRESERVE src0_sel:WORD_1 src1_sel:WORD_1
	v_mfma_f32_32x32x16_f16 a[176:191], v[110:113], v[66:69], a[176:191]
	v_cndmask_b32_e64 v38, v138, v156, s[52:53]
	s_mov_b64 vcc, s[54:55]
	v_cndmask_b32_sdwa v38, v138, v156, vcc dst_sel:WORD_1 dst_unused:UNUSED_PRESERVE src0_sel:WORD_1 src1_sel:WORD_1
	v_cndmask_b32_e64 v39, v138, v158, s[56:57]
	s_mov_b64 vcc, s[58:59]
	v_cndmask_b32_sdwa v39, v138, v158, vcc dst_sel:WORD_1 dst_unused:UNUSED_PRESERVE src0_sel:WORD_1 src1_sel:WORD_1
	v_mfma_f32_32x32x16_f16 a[112:127], v[114:117], v[70:73], a[112:127]
	v_cndmask_b32_e64 v40, v138, v160, s[60:61]
	s_mov_b64 vcc, s[62:63]
	v_cndmask_b32_sdwa v40, v138, v160, vcc dst_sel:WORD_1 dst_unused:UNUSED_PRESERVE src0_sel:WORD_1 src1_sel:WORD_1
	v_cndmask_b32_e64 v41, v138, v162, s[64:65]
	s_mov_b64 vcc, s[66:67]
	v_cndmask_b32_sdwa v41, v138, v162, vcc dst_sel:WORD_1 dst_unused:UNUSED_PRESERVE src0_sel:WORD_1 src1_sel:WORD_1
	v_mfma_f32_32x32x16_f16 a[160:175], v[110:113], v[70:73], a[160:175]
	v_pk_add_f16 v148, v19, v18
	v_pk_add_f16 v149, v20, v21
	v_mfma_f32_32x32x16_f16 a[128:143], v[114:117], v[78:81], a[128:143]
	v_pk_add_f16 v150, v39, v38
	v_pk_add_f16 v151, v40, v41
	v_mfma_f32_32x32x16_f16 a[144:159], v[110:113], v[78:81], a[144:159]
	v_pk_add_f16 v148, v148, v149
	v_pk_add_f16 v150, v150, v151
	v_mfma_f32_32x32x16_f16 a[80:95], v[114:117], v[102:105], a[80:95]
	v_dot2c_f32_f16_e32 v134, 0x3c003c00, v148
	v_dot2c_f32_f16_e32 v135, 0x3c003c00, v150
	v_mfma_f32_32x32x16_f16 a[96:111], v[110:113], v[102:105], a[96:111]
	s_add_i32 s92, s92, 0x9000
	s_cmp_lg_u32 s91, 2
	s_cselect_b32 s30, s92, 0
	s_add_u32 s20, s20, 0x100
	s_addc_u32 s21, s21, 0
	s_add_u32 s94, s94, 0x8000
	s_addc_u32 s95, s95, 0
	v_add_u32_e32 v145, 0x80, v145
	s_cmpk_eq_i32 s20, 0xf00
	s_mov_b32 s30, s91
	s_waitcnt vmcnt(0)
	s_waitcnt lgkmcnt(0)
	s_barrier
	s_cbranch_scc0 .LBB1_3
	v_accvgpr_read_b32 v175, a95
	v_accvgpr_read_b32 v174, a94
	v_accvgpr_read_b32 v173, a93
	v_accvgpr_read_b32 v172, a92
	v_accvgpr_read_b32 v171, a91
	v_accvgpr_read_b32 v170, a90
	v_accvgpr_read_b32 v169, a89
	v_accvgpr_read_b32 v168, a88
	v_accvgpr_read_b32 v167, a87
	v_accvgpr_read_b32 v166, a86
	v_accvgpr_read_b32 v165, a85
	v_accvgpr_read_b32 v164, a84
	v_accvgpr_read_b32 v163, a83
	v_accvgpr_read_b32 v162, a82
	v_accvgpr_read_b32 v161, a81
	v_accvgpr_read_b32 v160, a80
	v_mfma_f32_32x32x16_f16 a[80:95], v[18:21], v[74:77], a[0:15]
	s_nop 11
	v_accvgpr_read_b32 v159, a95
	v_accvgpr_read_b32 v158, a94
	v_accvgpr_read_b32 v157, a93
	v_accvgpr_read_b32 v156, a92
	v_accvgpr_read_b32 v155, a91
	v_accvgpr_read_b32 v154, a90
	v_accvgpr_read_b32 v153, a89
	v_accvgpr_read_b32 v152, a88
	v_accvgpr_read_b32 v151, a87
	v_accvgpr_read_b32 v150, a86
	v_accvgpr_read_b32 v149, a85
	v_accvgpr_read_b32 v148, a84
	v_accvgpr_read_b32 v147, a83
	v_accvgpr_read_b32 v146, a82
	v_accvgpr_read_b32 v145, a81
	v_accvgpr_read_b32 v144, a80
	ds_read_b128 v[2:5], v208 offset:28672
	ds_read_b128 v[82:85], v208
	ds_read_b128 v[58:61], v208 offset:4096
	ds_read_b128 v[50:53], v208 offset:8192
	ds_read_b128 v[26:29], v208 offset:12288
	ds_read_b128 v[22:25], v208 offset:16384
	ds_read_b128 v[14:17], v208 offset:20480
	ds_read_b128 v[10:13], v208 offset:24576
	s_load_dwordx16 s[68:83], s[0:1], 0xf80
	s_load_dwordx16 s[52:67], s[0:1], 0x8f80
	ds_read_b128 v[54:57], v142 offset:1984
	ds_read_b128 v[34:37], v143 offset:1984
	v_mfma_f32_32x32x16_f16 a[0:15], v[38:41], v[74:77], a[240:255]
	v_pk_mul_f16 v6, v46, v136
	v_pk_mul_f16 v7, v42, v137
	s_mov_b32 s20, 0x7060100
	v_pk_max_f16 v6, v6, v7
	s_nop 0
	v_cndmask_b32_e64 v7, v1, v6, s[36:37]
	v_mfma_f32_32x32x16_f16 a[240:255], v[18:21], v[126:129], a[16:31]
	v_cndmask_b32_e64 v6, v1, v6, s[38:39]
	v_perm_b32 v74, v6, v7, s20
	v_pk_mul_f16 v6, v47, v136
	v_pk_mul_f16 v7, v43, v137
	v_mfma_f32_32x32x16_f16 a[16:31], v[38:41], v[126:129], a[224:239]
	v_pk_max_f16 v6, v6, v7
	s_nop 0
	v_cndmask_b32_e64 v7, v1, v6, s[40:41]
	v_cndmask_b32_e64 v6, v1, v6, s[42:43]
	v_perm_b32 v75, v6, v7, s20
	v_mfma_f32_32x32x16_f16 a[224:239], v[18:21], v[122:125], a[32:47]
	v_pk_mul_f16 v6, v48, v136
	v_pk_mul_f16 v7, v44, v137
	s_nop 0
	v_pk_max_f16 v6, v6, v7
	s_nop 0
	v_cndmask_b32_e64 v7, v1, v6, s[44:45]
	v_mfma_f32_32x32x16_f16 a[32:47], v[38:41], v[122:125], a[208:223]
	v_cndmask_b32_e64 v6, v1, v6, s[46:47]
	v_perm_b32 v76, v6, v7, s20
	v_pk_mul_f16 v6, v49, v136
	v_pk_mul_f16 v7, v45, v137
	v_mfma_f32_32x32x16_f16 a[208:223], v[18:21], v[118:121], a[48:63]
	v_pk_max_f16 v6, v6, v7
	s_nop 0
	v_cndmask_b32_e64 v7, v1, v6, s[48:49]
	v_cndmask_b32_e64 v6, v1, v6, s[50:51]
	v_perm_b32 v77, v6, v7, s20
	v_mfma_f32_32x32x16_f16 a[48:63], v[38:41], v[118:121], a[192:207]
	v_pk_add_f16 v6, v75, v74
	v_pk_add_f16 v7, v76, v77
	s_nop 0
	v_pk_add_f16 v6, v6, v7
	s_nop 0
	v_dot2c_f32_f16_e32 v134, 0x3c003c00, v6
	v_mfma_f32_32x32x16_f16 a[192:207], v[18:21], v[106:109], a[64:79]
	v_pk_mul_f16 v6, v46, v140
	v_pk_mul_f16 v7, v42, v139
	s_nop 0
	v_pk_max_f16 v6, v6, v7
	s_nop 0
	v_cndmask_b32_e64 v7, v138, v6, s[4:5]
	v_mfma_f32_32x32x16_f16 a[64:79], v[38:41], v[106:109], a[176:191]
	v_pk_mul_f16 v8, v47, v140
	v_pk_mul_f16 v9, v43, v139
	v_cndmask_b32_e64 v6, v138, v6, s[6:7]
	v_pk_max_f16 v8, v8, v9
	v_mfma_f32_32x32x16_f16 a[176:191], v[18:21], v[98:101], a[112:127]
	v_pk_mul_f16 v30, v48, v140
	v_pk_mul_f16 v31, v44, v139
	v_cndmask_b32_e64 v9, v138, v8, s[8:9]
	v_cndmask_b32_e64 v8, v138, v8, s[10:11]
	v_mfma_f32_32x32x16_f16 a[112:127], v[38:41], v[98:101], a[160:175]
	v_pk_max_f16 v30, v30, v31
	v_pk_mul_f16 v32, v49, v140
	v_cndmask_b32_e64 v31, v138, v30, s[12:13]
	v_cndmask_b32_e64 v30, v138, v30, s[14:15]
	v_mfma_f32_32x32x16_f16 a[160:175], v[18:21], v[94:97], a[128:143]
	v_pk_mul_f16 v33, v45, v139
	s_nop 0
	v_pk_max_f16 v32, v32, v33
	s_nop 0
	v_cndmask_b32_e64 v33, v138, v32, s[16:17]
	v_cndmask_b32_e64 v32, v138, v32, s[18:19]
	v_mfma_f32_32x32x16_f16 a[128:143], v[38:41], v[94:97], a[144:159]
	v_perm_b32 v78, v6, v7, s20
	v_perm_b32 v79, v8, v9, s20
	v_perm_b32 v80, v30, v31, s20
	v_perm_b32 v81, v32, v33, s20
	v_pk_add_f16 v6, v79, v78
	v_pk_add_f16 v7, v80, v81
	v_accvgpr_write_b32 a80, v160
	v_pk_add_f16 v6, v6, v7
	v_accvgpr_write_b32 a81, v161
	v_accvgpr_write_b32 a82, v162
	v_accvgpr_write_b32 a83, v163
	v_accvgpr_write_b32 a84, v164
	v_accvgpr_write_b32 a85, v165
	v_accvgpr_write_b32 a86, v166
	v_accvgpr_write_b32 a87, v167
	v_accvgpr_write_b32 a88, v168
	v_accvgpr_write_b32 a89, v169
	v_accvgpr_write_b32 a90, v170
	v_accvgpr_write_b32 a91, v171
	v_accvgpr_write_b32 a92, v172
	v_accvgpr_write_b32 a93, v173
	v_accvgpr_write_b32 a94, v174
	v_accvgpr_write_b32 a95, v175
	v_dot2c_f32_f16_e32 v135, 0x3c003c00, v6
	s_nop 0
	v_mfma_f32_32x32x16_f16 a[144:159], v[18:21], v[86:89], a[80:95]
	v_mfma_f32_32x32x16_f16 a[80:95], v[38:41], v[86:89], a[96:111]
	s_nop 6
	v_accvgpr_write_b32 a96, v144
	v_accvgpr_write_b32 a97, v145
	v_accvgpr_write_b32 a98, v146
	v_accvgpr_write_b32 a99, v147
	v_accvgpr_write_b32 a100, v148
	v_accvgpr_write_b32 a101, v149
	v_accvgpr_write_b32 a102, v150
	v_accvgpr_write_b32 a103, v151
	v_accvgpr_write_b32 a104, v152
	v_accvgpr_write_b32 a105, v153
	v_accvgpr_write_b32 a106, v154
	v_accvgpr_write_b32 a107, v155
	v_accvgpr_write_b32 a108, v156
	v_accvgpr_write_b32 a109, v157
	v_accvgpr_write_b32 a110, v158
	v_accvgpr_write_b32 a111, v159
	s_waitcnt lgkmcnt(0)
	s_nop 0
	v_mfma_f32_32x32x16_f16 a[96:111], v[74:77], v[82:85], a[96:111]
	ds_read_b128 v[86:89], v209
	ds_read_b128 v[70:73], v209 offset:4096
	ds_read_b128 v[62:65], v209 offset:8192
	ds_read_b128 v[42:45], v209 offset:12288
	ds_read_b128 v[38:41], v209 offset:16384
	ds_read_b128 v[30:33], v209 offset:20480
	ds_read_b128 v[18:21], v209 offset:24576
	ds_read_b128 v[6:9], v209 offset:28672
	s_load_dwordx16 s[36:51], s[0:1], 0xfc0
	s_load_dwordx16 s[4:19], s[0:1], 0x8fc0
	ds_read_b128 v[66:69], v142 offset:2016
	ds_read_b128 v[46:49], v143 offset:2016
	v_mfma_f32_32x32x16_f16 a[0:15], v[78:81], v[82:85], a[0:15]
	v_pk_mul_f16 v82, v54, v136
	v_pk_mul_f16 v83, v34, v137
	s_nop 0
	v_pk_max_f16 v82, v82, v83
	s_nop 0
	v_cndmask_b32_e64 v83, v1, v82, s[68:69]
	v_mfma_f32_32x32x16_f16 a[240:255], v[74:77], v[58:61], a[240:255]
	v_cndmask_b32_e64 v82, v1, v82, s[70:71]
	v_perm_b32 v82, v82, v83, s20
	v_pk_mul_f16 v83, v55, v136
	v_pk_mul_f16 v84, v35, v137
	v_mfma_f32_32x32x16_f16 a[16:31], v[78:81], v[58:61], a[16:31]
	v_pk_max_f16 v58, v83, v84
	s_nop 0
	v_cndmask_b32_e64 v59, v1, v58, s[72:73]
	v_cndmask_b32_e64 v58, v1, v58, s[74:75]
	v_perm_b32 v83, v58, v59, s20
	v_mfma_f32_32x32x16_f16 a[224:239], v[74:77], v[50:53], a[224:239]
	v_pk_mul_f16 v58, v56, v136
	v_pk_mul_f16 v59, v36, v137
	s_nop 0
	v_pk_max_f16 v58, v58, v59
	s_nop 0
	v_cndmask_b32_e64 v59, v1, v58, s[76:77]
	v_mfma_f32_32x32x16_f16 a[32:47], v[78:81], v[50:53], a[32:47]
	v_cndmask_b32_e64 v50, v1, v58, s[78:79]
	v_perm_b32 v84, v50, v59, s20
	v_pk_mul_f16 v50, v57, v136
	v_pk_mul_f16 v51, v37, v137
	v_mfma_f32_32x32x16_f16 a[208:223], v[74:77], v[26:29], a[208:223]
	v_pk_max_f16 v50, v50, v51
	s_nop 0
	v_cndmask_b32_e64 v51, v1, v50, s[80:81]
	v_cndmask_b32_e64 v50, v1, v50, s[82:83]
	v_perm_b32 v85, v50, v51, s20
	v_mfma_f32_32x32x16_f16 a[48:63], v[78:81], v[26:29], a[48:63]
	v_pk_add_f16 v26, v83, v82
	v_pk_add_f16 v27, v84, v85
	s_nop 0
	v_pk_add_f16 v26, v26, v27
	s_nop 0
	v_dot2c_f32_f16_e32 v134, 0x3c003c00, v26
	v_mfma_f32_32x32x16_f16 a[192:207], v[74:77], v[22:25], a[192:207]
	v_pk_mul_f16 v26, v54, v140
	v_pk_mul_f16 v27, v34, v139
	s_nop 0
	v_pk_max_f16 v26, v26, v27
	s_nop 0
	v_cndmask_b32_e64 v27, v138, v26, s[52:53]
	v_mfma_f32_32x32x16_f16 a[64:79], v[78:81], v[22:25], a[64:79]
	v_pk_mul_f16 v23, v55, v140
	v_pk_mul_f16 v24, v35, v139
	v_cndmask_b32_e64 v22, v138, v26, s[54:55]
	v_pk_max_f16 v23, v23, v24
	v_mfma_f32_32x32x16_f16 a[176:191], v[74:77], v[14:17], a[176:191]
	v_pk_mul_f16 v25, v56, v140
	v_pk_mul_f16 v26, v36, v139
	v_cndmask_b32_e64 v24, v138, v23, s[56:57]
	v_cndmask_b32_e64 v23, v138, v23, s[58:59]
	v_mfma_f32_32x32x16_f16 a[112:127], v[78:81], v[14:17], a[112:127]
	v_pk_max_f16 v14, v25, v26
	v_pk_mul_f16 v16, v57, v140
	v_cndmask_b32_e64 v15, v138, v14, s[60:61]
	v_cndmask_b32_e64 v14, v138, v14, s[62:63]
	v_mfma_f32_32x32x16_f16 a[160:175], v[74:77], v[10:13], a[160:175]
	v_pk_mul_f16 v17, v37, v139
	s_nop 0
	v_pk_max_f16 v16, v16, v17
	s_nop 0
	v_cndmask_b32_e64 v17, v138, v16, s[64:65]
	v_cndmask_b32_e64 v16, v138, v16, s[66:67]
	v_mfma_f32_32x32x16_f16 a[128:143], v[78:81], v[10:13], a[128:143]
	v_perm_b32 v10, v22, v27, s20
	v_perm_b32 v11, v23, v24, s20
	v_perm_b32 v12, v14, v15, s20
	v_perm_b32 v13, v16, v17, s20
	v_mfma_f32_32x32x16_f16 a[144:159], v[74:77], v[2:5], a[144:159]
	v_pk_add_f16 v14, v11, v10
	v_pk_add_f16 v15, v12, v13
	s_nop 0
	v_pk_add_f16 v14, v14, v15
	s_nop 0
	v_dot2c_f32_f16_e32 v135, 0x3c003c00, v14
	v_mfma_f32_32x32x16_f16 a[80:95], v[78:81], v[2:5], a[80:95]
	s_waitcnt lgkmcnt(0)
	v_mfma_f32_32x32x16_f16 a[96:111], v[82:85], v[86:89], a[96:111]
	ds_read_b128 v[2:5], v210
	ds_read_b128 v[14:17], v210 offset:4096
	ds_read_b128 v[22:25], v210 offset:8192
	ds_read_b128 v[26:29], v210 offset:12288
	ds_read_b128 v[34:37], v210 offset:16384
	ds_read_b128 v[50:53], v210 offset:20480
	ds_read_b128 v[54:57], v210 offset:24576
	ds_read_b128 v[58:61], v210 offset:28672
	v_mfma_f32_32x32x16_f16 a[0:15], v[10:13], v[86:89], a[0:15]
	v_pk_mul_f16 v74, v136, v66
	v_pk_mul_f16 v75, v137, v46
	s_nop 0
	v_pk_max_f16 v74, v74, v75
	s_nop 0
	v_cndmask_b32_e64 v75, v1, v74, s[36:37]
	v_mfma_f32_32x32x16_f16 a[240:255], v[82:85], v[70:73], a[240:255]
	v_cndmask_b32_e64 v74, v1, v74, s[38:39]
	v_perm_b32 v74, v74, v75, s20
	v_pk_mul_f16 v75, v136, v67
	v_pk_mul_f16 v76, v137, v47
	v_mfma_f32_32x32x16_f16 a[16:31], v[10:13], v[70:73], a[16:31]
	v_pk_max_f16 v70, v75, v76
	s_nop 0
	v_cndmask_b32_e64 v71, v1, v70, s[40:41]
	v_cndmask_b32_e64 v70, v1, v70, s[42:43]
	v_perm_b32 v75, v70, v71, s20
	v_mfma_f32_32x32x16_f16 a[224:239], v[82:85], v[62:65], a[224:239]
	v_pk_mul_f16 v70, v136, v68
	v_pk_mul_f16 v71, v137, v48
	s_nop 0
	v_pk_max_f16 v70, v70, v71
	s_nop 0
	v_cndmask_b32_e64 v71, v1, v70, s[44:45]
	v_mfma_f32_32x32x16_f16 a[32:47], v[10:13], v[62:65], a[32:47]
	v_cndmask_b32_e64 v62, v1, v70, s[46:47]
	v_perm_b32 v76, v62, v71, s20
	v_pk_mul_f16 v62, v136, v69
	v_pk_mul_f16 v63, v137, v49
	v_mfma_f32_32x32x16_f16 a[208:223], v[82:85], v[42:45], a[208:223]
	v_pk_max_f16 v62, v62, v63
	s_nop 0
	v_cndmask_b32_e64 v63, v1, v62, s[48:49]
	v_cndmask_b32_e64 v1, v1, v62, s[50:51]
	v_perm_b32 v77, v1, v63, s20
	v_mfma_f32_32x32x16_f16 a[48:63], v[10:13], v[42:45], a[48:63]
	v_pk_add_f16 v1, v75, v74
	v_pk_add_f16 v42, v76, v77
	s_nop 0
	v_pk_add_f16 v1, v1, v42
	s_nop 0
	v_dot2c_f32_f16_e32 v134, 0x3c003c00, v1
	v_mfma_f32_32x32x16_f16 a[192:207], v[82:85], v[38:41], a[192:207]
	v_pk_mul_f16 v1, v140, v66
	v_pk_mul_f16 v42, v139, v46
	s_nop 0
	v_pk_max_f16 v1, v1, v42
	s_nop 0
	v_cndmask_b32_e64 v42, v138, v1, s[4:5]
	v_mfma_f32_32x32x16_f16 a[64:79], v[10:13], v[38:41], a[64:79]
	v_pk_mul_f16 v38, v140, v67
	v_pk_mul_f16 v39, v139, v47
	v_cndmask_b32_e64 v1, v138, v1, s[6:7]
	v_pk_max_f16 v38, v38, v39
	v_mfma_f32_32x32x16_f16 a[176:191], v[82:85], v[30:33], a[176:191]
	v_pk_mul_f16 v40, v140, v68
	v_pk_mul_f16 v41, v139, v48
	v_cndmask_b32_e64 v39, v138, v38, s[8:9]
	v_cndmask_b32_e64 v38, v138, v38, s[10:11]
	v_mfma_f32_32x32x16_f16 a[112:127], v[10:13], v[30:33], a[112:127]
	v_pk_max_f16 v30, v40, v41
	v_pk_mul_f16 v32, v140, v69
	v_cndmask_b32_e64 v31, v138, v30, s[12:13]
	v_cndmask_b32_e64 v30, v138, v30, s[14:15]
	v_mfma_f32_32x32x16_f16 a[160:175], v[82:85], v[18:21], a[160:175]
	v_pk_mul_f16 v33, v139, v49
	s_nop 0
	v_pk_max_f16 v32, v32, v33
	s_nop 0
	v_cndmask_b32_e64 v33, v138, v32, s[16:17]
	v_cndmask_b32_e64 v32, v138, v32, s[18:19]
	v_mfma_f32_32x32x16_f16 a[128:143], v[10:13], v[18:21], a[128:143]
	v_perm_b32 v18, v1, v42, s20
	v_perm_b32 v19, v38, v39, s20
	v_perm_b32 v20, v30, v31, s20
	v_perm_b32 v21, v32, v33, s20
	v_mfma_f32_32x32x16_f16 a[144:159], v[82:85], v[6:9], a[144:159]
	v_pk_add_f16 v1, v19, v18
	v_pk_add_f16 v30, v20, v21
	s_nop 0
	v_pk_add_f16 v1, v1, v30
	s_nop 0
	v_dot2c_f32_f16_e32 v135, 0x3c003c00, v1
	v_mfma_f32_32x32x16_f16 a[80:95], v[10:13], v[6:9], a[80:95]
	s_waitcnt lgkmcnt(7)
	v_mfma_f32_32x32x16_f16 a[96:111], v[74:77], v[2:5], a[96:111]
	v_mfma_f32_32x32x16_f16 a[0:15], v[18:21], v[2:5], a[0:15]
	s_waitcnt lgkmcnt(6)
	v_mfma_f32_32x32x16_f16 a[240:255], v[74:77], v[14:17], a[240:255]
	v_mfma_f32_32x32x16_f16 a[16:31], v[18:21], v[14:17], a[16:31]
	s_waitcnt lgkmcnt(5)
	v_mfma_f32_32x32x16_f16 a[224:239], v[74:77], v[22:25], a[224:239]
	v_mfma_f32_32x32x16_f16 a[32:47], v[18:21], v[22:25], a[32:47]
	s_waitcnt lgkmcnt(4)
	v_mfma_f32_32x32x16_f16 a[208:223], v[74:77], v[26:29], a[208:223]
	v_mfma_f32_32x32x16_f16 a[48:63], v[18:21], v[26:29], a[48:63]
	s_waitcnt lgkmcnt(3)
	v_mfma_f32_32x32x16_f16 a[192:207], v[74:77], v[34:37], a[192:207]
	v_mfma_f32_32x32x16_f16 a[64:79], v[18:21], v[34:37], a[64:79]
	s_waitcnt lgkmcnt(2)
	v_mfma_f32_32x32x16_f16 a[176:191], v[74:77], v[50:53], a[176:191]
	v_mfma_f32_32x32x16_f16 a[112:127], v[18:21], v[50:53], a[112:127]
	s_waitcnt lgkmcnt(1)
	v_mfma_f32_32x32x16_f16 a[160:175], v[74:77], v[54:57], a[160:175]
	v_mfma_f32_32x32x16_f16 a[128:143], v[18:21], v[54:57], a[128:143]
	s_waitcnt lgkmcnt(0)
	v_mfma_f32_32x32x16_f16 a[144:159], v[74:77], v[58:61], a[144:159]
	v_mfma_f32_32x32x16_f16 a[80:95], v[18:21], v[58:61], a[80:95]
	v_readfirstlane_b32 s1, v0
	s_and_b32 s0, s3, 0xffffff00
	s_andn2_b32 s1, s1, 63
	s_add_i32 s4, s1, s0
	s_lshl_b32 s0, s2, 13
	s_and_b32 s6, s0, 0xe000
	s_ashr_i32 s5, s4, 31
	s_add_u32 s0, s4, s6
	s_addc_u32 s1, s5, 0
	s_lshl_b64 s[2:3], s[0:1], 9
	v_lshrrev_b32_e32 v0, 3, v132
	s_add_u32 s2, s22, s2
	v_and_b32_e32 v3, 12, v0
	s_addc_u32 s3, s23, s3
	v_lshlrev_b32_e32 v0, 9, v3
	v_mov_b32_e32 v1, 0
	v_lshl_add_u64 v[4:5], s[2:3], 0, v[0:1]
	v_lshlrev_b32_e32 v0, 4, v132
	v_and_b32_e32 v0, 0x1f0, v0
	v_lshl_add_u64 v[4:5], v[4:5], 0, v[0:1]
	v_accvgpr_read_b32 v6, a96
	v_accvgpr_read_b32 v7, a240
	v_accvgpr_read_b32 v8, a224
	v_max3_f32 v0, |v6|, |v7|, |v8|
	v_accvgpr_read_b32 v9, a208
	v_accvgpr_read_b32 v14, a192
	v_max3_f32 v0, |v0|, |v9|, |v14|
	v_accvgpr_read_b32 v15, a176
	v_accvgpr_read_b32 v16, a160
	v_max3_f32 v0, |v0|, |v15|, |v16|
	v_accvgpr_read_b32 v17, a144
	v_max3_f32 v10, |v0|, |v17|, |v17|
	v_accvgpr_read_b32 v18, a97
	v_accvgpr_read_b32 v19, a241
	v_accvgpr_read_b32 v20, a225
	v_max3_f32 v0, |v18|, |v19|, |v20|
	v_accvgpr_read_b32 v21, a209
	v_accvgpr_read_b32 v22, a193
	v_max3_f32 v0, |v0|, |v21|, |v22|
	v_accvgpr_read_b32 v23, a177
	v_accvgpr_read_b32 v24, a161
	v_max3_f32 v0, |v0|, |v23|, |v24|
	v_accvgpr_read_b32 v25, a145
	v_max3_f32 v11, |v0|, |v25|, |v25|
	v_accvgpr_read_b32 v26, a98
	v_accvgpr_read_b32 v27, a242
	v_accvgpr_read_b32 v28, a226
	v_max3_f32 v0, |v26|, |v27|, |v28|
	v_accvgpr_read_b32 v29, a210
	v_accvgpr_read_b32 v30, a194
	v_max3_f32 v0, |v0|, |v29|, |v30|
	v_accvgpr_read_b32 v31, a178
	v_accvgpr_read_b32 v32, a162
	v_max3_f32 v0, |v0|, |v31|, |v32|
	v_accvgpr_read_b32 v33, a146
	v_max3_f32 v12, |v0|, |v33|, |v33|
	v_accvgpr_read_b32 v34, a99
	v_accvgpr_read_b32 v35, a243
	v_accvgpr_read_b32 v36, a227
	v_max3_f32 v0, |v34|, |v35|, |v36|
	v_accvgpr_read_b32 v37, a211
	v_accvgpr_read_b32 v38, a195
	v_max3_f32 v0, |v0|, |v37|, |v38|
	v_accvgpr_read_b32 v39, a179
	v_accvgpr_read_b32 v40, a163
	v_max3_f32 v0, |v0|, |v39|, |v40|
	v_accvgpr_read_b32 v41, a147
	v_max3_f32 v13, |v0|, |v41|, |v41|
	v_lshlrev_b32_e32 v0, 2, v3
	s_nop 1
	v_max_f32_dpp v10, v10, v10 quad_perm:[1,0,3,2] row_mask:0xf bank_mask:0xf
	v_max_f32_dpp v11, v11, v11 quad_perm:[1,0,3,2] row_mask:0xf bank_mask:0xf
	v_max_f32_dpp v12, v12, v12 quad_perm:[1,0,3,2] row_mask:0xf bank_mask:0xf
	v_max_f32_dpp v13, v13, v13 quad_perm:[1,0,3,2] row_mask:0xf bank_mask:0xf
	v_max_f32_dpp v10, v10, v10 quad_perm:[2,3,0,1] row_mask:0xf bank_mask:0xf
	v_max_f32_dpp v11, v11, v11 quad_perm:[2,3,0,1] row_mask:0xf bank_mask:0xf
	v_max_f32_dpp v12, v12, v12 quad_perm:[2,3,0,1] row_mask:0xf bank_mask:0xf
	v_max_f32_dpp v13, v13, v13 quad_perm:[2,3,0,1] row_mask:0xf bank_mask:0xf
	v_max_f32_dpp v10, v10, v10 row_half_mirror row_mask:0xf bank_mask:0xf
	v_max_f32_dpp v11, v11, v11 row_half_mirror row_mask:0xf bank_mask:0xf
	v_max_f32_dpp v12, v12, v12 row_half_mirror row_mask:0xf bank_mask:0xf
	v_max_f32_dpp v13, v13, v13 row_half_mirror row_mask:0xf bank_mask:0xf
	v_max_f32_dpp v10, v10, v10 row_mirror row_mask:0xf bank_mask:0xf
	v_max_f32_dpp v11, v11, v11 row_mirror row_mask:0xf bank_mask:0xf
	v_max_f32_dpp v12, v12, v12 row_mirror row_mask:0xf bank_mask:0xf
	v_max_f32_dpp v13, v13, v13 row_mirror row_mask:0xf bank_mask:0xf
	s_nop 0
	ds_swizzle_b32 v232, v10 offset:swizzle(SWAP,16)
	ds_swizzle_b32 v233, v12 offset:swizzle(SWAP,16)
	ds_swizzle_b32 v234, v11 offset:swizzle(SWAP,16)
	ds_swizzle_b32 v235, v13 offset:swizzle(SWAP,16)
	s_waitcnt lgkmcnt(0)
	v_max_f32_e32 v10, v10, v232
	v_rcp_f32_e32 v42, v10
	v_cmp_lt_f32_e32 vcc, 0, v10
	s_waitcnt lgkmcnt(0)
	v_max_f32_e32 v12, v12, v233
	s_waitcnt lgkmcnt(0)
	v_max_f32_e32 v11, v11, v234
	s_lshl_b32 s2, s6, 2
	v_cndmask_b32_e32 v3, 0, v42, vcc
	v_pk_mul_f32 v[224:225], v[6:7], v[2:3] op_sel:[0,1] op_sel_hi:[1,1]
	v_pk_mul_f32 v[226:227], v[8:9], v[2:3] op_sel:[0,1] op_sel_hi:[1,1]
	v_cvt_pknorm_i16_f32 v6, v224, v225
	v_cvt_pknorm_i16_f32 v7, v226, v227
	v_pk_mul_f32 v[228:229], v[14:15], v[2:3] op_sel:[0,1] op_sel_hi:[1,1]
	v_rcp_f32_e32 v14, v11
	v_cvt_pknorm_i16_f32 v8, v228, v229
	v_pk_mul_f32 v[230:231], v[16:17], v[2:3] op_sel:[0,1] op_sel_hi:[1,1]
	v_cmp_lt_f32_e32 vcc, 0, v11
	v_cvt_pknorm_i16_f32 v9, v230, v231
	global_store_dwordx4 v[4:5], v[6:9], off sc0 sc1
	s_add_u32 s6, s24, s2
	v_cndmask_b32_e32 v3, 0, v14, vcc
	v_pk_mul_f32 v[224:225], v[18:19], v[2:3] op_sel:[0,1] op_sel_hi:[1,1]
	v_pk_mul_f32 v[226:227], v[20:21], v[2:3] op_sel:[0,1] op_sel_hi:[1,1]
	v_cvt_pknorm_i16_f32 v6, v224, v225
	v_cvt_pknorm_i16_f32 v7, v226, v227
	v_pk_mul_f32 v[228:229], v[22:23], v[2:3] op_sel:[0,1] op_sel_hi:[1,1]
	v_pk_mul_f32 v[230:231], v[24:25], v[2:3] op_sel:[0,1] op_sel_hi:[1,1]
	v_cvt_pknorm_i16_f32 v8, v228, v229
	v_cvt_pknorm_i16_f32 v9, v230, v231
	v_rcp_f32_e32 v3, v12
	s_addc_u32 s7, s25, 0
	s_lshl_b64 s[2:3], s[4:5], 2
	s_mov_b64 s[4:5], 0x200
	s_add_u32 s2, s6, s2
	v_lshl_add_u64 v[14:15], v[4:5], 0, s[4:5]
	s_mov_b32 s4, 0x38000100
	v_cmp_lt_f32_e32 vcc, 0, v12
	s_addc_u32 s3, s7, s3
	global_store_dwordx4 v[14:15], v[6:9], off sc0 sc1
	s_nop 1
	v_pk_mul_f32 v[6:7], v[10:11], s[4:5] op_sel_hi:[1,0]
	v_cndmask_b32_e32 v3, 0, v3, vcc
	global_store_dwordx2 v0, v[6:7], s[2:3]
	v_pk_mul_f32 v[224:225], v[26:27], v[2:3] op_sel:[0,1] op_sel_hi:[1,1]
	v_pk_mul_f32 v[226:227], v[28:29], v[2:3] op_sel:[0,1] op_sel_hi:[1,1]
	v_cvt_pknorm_i16_f32 v6, v224, v225
	v_cvt_pknorm_i16_f32 v7, v226, v227
	v_pk_mul_f32 v[228:229], v[30:31], v[2:3] op_sel:[0,1] op_sel_hi:[1,1]
	v_pk_mul_f32 v[230:231], v[32:33], v[2:3] op_sel:[0,1] op_sel_hi:[1,1]
	v_cvt_pknorm_i16_f32 v8, v228, v229
	s_waitcnt lgkmcnt(0)
	v_max_f32_e32 v13, v13, v235
	v_cvt_pknorm_i16_f32 v9, v230, v231
	v_rcp_f32_e32 v3, v13
	v_cmp_lt_f32_e32 vcc, 0, v13
	s_mov_b64 s[6:7], 0x400
	v_lshl_add_u64 v[10:11], v[4:5], 0, s[6:7]
	v_cndmask_b32_e32 v3, 0, v3, vcc
	global_store_dwordx4 v[10:11], v[6:9], off sc0 sc1
	v_pk_mul_f32 v[224:225], v[34:35], v[2:3] op_sel:[0,1] op_sel_hi:[1,1]
	v_pk_mul_f32 v[226:227], v[36:37], v[2:3] op_sel:[0,1] op_sel_hi:[1,1]
	v_cvt_pknorm_i16_f32 v6, v224, v225
	v_cvt_pknorm_i16_f32 v7, v226, v227
	v_pk_mul_f32 v[228:229], v[38:39], v[2:3] op_sel:[0,1] op_sel_hi:[1,1]
	v_pk_mul_f32 v[230:231], v[40:41], v[2:3] op_sel:[0,1] op_sel_hi:[1,1]
	v_cvt_pknorm_i16_f32 v8, v228, v229
	s_mov_b64 s[6:7], 0x600
	v_cvt_pknorm_i16_f32 v9, v230, v231
	v_lshl_add_u64 v[10:11], v[4:5], 0, s[6:7]
	global_store_dwordx4 v[10:11], v[6:9], off sc0 sc1
	s_nop 1
	v_pk_mul_f32 v[6:7], v[12:13], s[4:5] op_sel_hi:[1,0]
	v_lshlrev_b32_e32 v2, 2, v132
	global_store_dwordx2 v0, v[6:7], s[2:3] offset:8
	v_accvgpr_read_b32 v42, a100
	v_accvgpr_read_b32 v6, a244
	v_accvgpr_read_b32 v7, a228
	v_max3_f32 v8, |v42|, |v6|, |v7|
	v_accvgpr_read_b32 v9, a212
	v_accvgpr_read_b32 v14, a196
	v_max3_f32 v8, |v8|, |v9|, |v14|
	v_accvgpr_read_b32 v15, a180
	v_accvgpr_read_b32 v16, a164
	v_max3_f32 v8, |v8|, |v15|, |v16|
	v_accvgpr_read_b32 v10, a148
	v_accvgpr_read_b32 v43, a101
	v_accvgpr_read_b32 v17, a148
	v_max3_f32 v8, |v8|, |v17|, |v10|
	v_accvgpr_read_b32 v19, a245
	v_accvgpr_read_b32 v20, a229
	v_max3_f32 v10, |v43|, |v19|, |v20|
	v_accvgpr_read_b32 v21, a213
	v_accvgpr_read_b32 v22, a197
	v_max3_f32 v10, |v10|, |v21|, |v22|
	v_accvgpr_read_b32 v23, a181
	v_accvgpr_read_b32 v24, a165
	v_max3_f32 v10, |v10|, |v23|, |v24|
	v_accvgpr_read_b32 v44, a102
	v_accvgpr_read_b32 v25, a149
	v_max3_f32 v11, |v10|, |v25|, |v25|
	v_accvgpr_read_b32 v27, a246
	v_accvgpr_read_b32 v28, a230
	v_max3_f32 v10, |v44|, |v27|, |v28|
	v_accvgpr_read_b32 v29, a214
	v_accvgpr_read_b32 v30, a198
	v_max3_f32 v10, |v10|, |v29|, |v30|
	v_accvgpr_read_b32 v31, a182
	v_accvgpr_read_b32 v32, a166
	v_max3_f32 v10, |v10|, |v31|, |v32|
	v_accvgpr_read_b32 v45, a103
	v_accvgpr_read_b32 v33, a150
	v_max3_f32 v12, |v10|, |v33|, |v33|
	v_accvgpr_read_b32 v35, a247
	v_accvgpr_read_b32 v36, a231
	v_max3_f32 v10, |v45|, |v35|, |v36|
	v_accvgpr_read_b32 v37, a215
	v_accvgpr_read_b32 v38, a199
	v_max3_f32 v10, |v10|, |v37|, |v38|
	v_accvgpr_read_b32 v39, a183
	v_accvgpr_read_b32 v40, a167
	v_max3_f32 v10, |v10|, |v39|, |v40|
	v_accvgpr_read_b32 v41, a151
	v_max3_f32 v13, |v10|, |v41|, |v41|
	v_mov_b32_e32 v3, v42
	s_nop 1
	v_max_f32_dpp v8, v8, v8 quad_perm:[1,0,3,2] row_mask:0xf bank_mask:0xf
	v_max_f32_dpp v11, v11, v11 quad_perm:[1,0,3,2] row_mask:0xf bank_mask:0xf
	v_max_f32_dpp v12, v12, v12 quad_perm:[1,0,3,2] row_mask:0xf bank_mask:0xf
	v_max_f32_dpp v13, v13, v13 quad_perm:[1,0,3,2] row_mask:0xf bank_mask:0xf
	v_max_f32_dpp v8, v8, v8 quad_perm:[2,3,0,1] row_mask:0xf bank_mask:0xf
	v_max_f32_dpp v11, v11, v11 quad_perm:[2,3,0,1] row_mask:0xf bank_mask:0xf
	v_max_f32_dpp v12, v12, v12 quad_perm:[2,3,0,1] row_mask:0xf bank_mask:0xf
	v_max_f32_dpp v13, v13, v13 quad_perm:[2,3,0,1] row_mask:0xf bank_mask:0xf
	v_max_f32_dpp v8, v8, v8 row_half_mirror row_mask:0xf bank_mask:0xf
	v_max_f32_dpp v11, v11, v11 row_half_mirror row_mask:0xf bank_mask:0xf
	v_max_f32_dpp v12, v12, v12 row_half_mirror row_mask:0xf bank_mask:0xf
	v_max_f32_dpp v13, v13, v13 row_half_mirror row_mask:0xf bank_mask:0xf
	v_max_f32_dpp v8, v8, v8 row_mirror row_mask:0xf bank_mask:0xf
	v_max_f32_dpp v11, v11, v11 row_mirror row_mask:0xf bank_mask:0xf
	v_max_f32_dpp v12, v12, v12 row_mirror row_mask:0xf bank_mask:0xf
	v_max_f32_dpp v13, v13, v13 row_mirror row_mask:0xf bank_mask:0xf
	s_nop 0
	ds_swizzle_b32 v232, v8 offset:swizzle(SWAP,16)
	ds_swizzle_b32 v233, v11 offset:swizzle(SWAP,16)
	ds_swizzle_b32 v234, v12 offset:swizzle(SWAP,16)
	ds_swizzle_b32 v235, v13 offset:swizzle(SWAP,16)
	s_waitcnt lgkmcnt(0)
	v_max_f32_e32 v10, v8, v232
	v_rcp_f32_e32 v8, v10
	v_cmp_lt_f32_e32 vcc, 0, v10
	s_waitcnt lgkmcnt(0)
	v_max_f32_e32 v11, v11, v233
	v_mov_b32_e32 v18, v43
	s_mov_b64 s[6:7], 0x1000
	v_cndmask_b32_e32 v42, 0, v8, vcc
	v_mul_f32_e32 v3, v42, v3
	v_mul_f32_e32 v6, v42, v6
	v_cvt_pknorm_i16_f32 v6, v3, v6
	v_mul_f32_e32 v3, v42, v7
	v_mul_f32_e32 v7, v42, v9
	v_cvt_pknorm_i16_f32 v7, v3, v7
	v_pk_mul_f32 v[224:225], v[14:15], v[42:43] op_sel_hi:[1,0]
	v_pk_mul_f32 v[226:227], v[16:17], v[42:43] op_sel_hi:[1,0]
	v_cvt_pknorm_i16_f32 v8, v224, v225
	v_cvt_pknorm_i16_f32 v9, v226, v227
	v_rcp_f32_e32 v3, v11
	v_cmp_lt_f32_e32 vcc, 0, v11
	v_lshl_add_u64 v[14:15], v[4:5], 0, s[6:7]
	global_store_dwordx4 v[14:15], v[6:9], off sc0 sc1
	v_cndmask_b32_e32 v3, 0, v3, vcc
	v_pk_mul_f32 v[228:229], v[18:19], v[2:3] op_sel:[0,1] op_sel_hi:[1,1]
	v_pk_mul_f32 v[230:231], v[20:21], v[2:3] op_sel:[0,1] op_sel_hi:[1,1]
	v_cvt_pknorm_i16_f32 v6, v228, v229
	v_cvt_pknorm_i16_f32 v7, v230, v231
	v_pk_mul_f32 v[224:225], v[22:23], v[2:3] op_sel:[0,1] op_sel_hi:[1,1]
	v_pk_mul_f32 v[226:227], v[24:25], v[2:3] op_sel:[0,1] op_sel_hi:[1,1]
	v_cvt_pknorm_i16_f32 v8, v224, v225
	s_waitcnt lgkmcnt(0)
	v_max_f32_e32 v12, v12, v234
	v_cvt_pknorm_i16_f32 v9, v226, v227
	v_rcp_f32_e32 v3, v12
	s_mov_b64 s[6:7], 0x1200
	v_cmp_lt_f32_e32 vcc, 0, v12
	v_mov_b32_e32 v26, v44
	v_lshl_add_u64 v[14:15], v[4:5], 0, s[6:7]
	global_store_dwordx4 v[14:15], v[6:9], off sc0 sc1
	s_nop 1
	v_pk_mul_f32 v[6:7], v[10:11], s[4:5] op_sel_hi:[1,0]
	v_cndmask_b32_e32 v3, 0, v3, vcc
	global_store_dwordx2 v0, v[6:7], s[2:3] offset:32
	v_pk_mul_f32 v[228:229], v[26:27], v[2:3] op_sel:[0,1] op_sel_hi:[1,1]
	v_pk_mul_f32 v[230:231], v[28:29], v[2:3] op_sel:[0,1] op_sel_hi:[1,1]
	v_cvt_pknorm_i16_f32 v6, v228, v229
	v_cvt_pknorm_i16_f32 v7, v230, v231
	v_pk_mul_f32 v[224:225], v[30:31], v[2:3] op_sel:[0,1] op_sel_hi:[1,1]
	v_pk_mul_f32 v[226:227], v[32:33], v[2:3] op_sel:[0,1] op_sel_hi:[1,1]
	v_cvt_pknorm_i16_f32 v8, v224, v225
	s_waitcnt lgkmcnt(0)
	v_max_f32_e32 v13, v13, v235
	v_cvt_pknorm_i16_f32 v9, v226, v227
	v_rcp_f32_e32 v3, v13
	v_cmp_lt_f32_e32 vcc, 0, v13
	v_mov_b32_e32 v34, v45
	s_mov_b64 s[6:7], 0x1400
	v_cndmask_b32_e32 v3, 0, v3, vcc
	v_lshl_add_u64 v[10:11], v[4:5], 0, s[6:7]
	global_store_dwordx4 v[10:11], v[6:9], off sc0 sc1
	v_pk_mul_f32 v[228:229], v[34:35], v[2:3] op_sel:[0,1] op_sel_hi:[1,1]
	v_pk_mul_f32 v[230:231], v[36:37], v[2:3] op_sel:[0,1] op_sel_hi:[1,1]
	v_cvt_pknorm_i16_f32 v6, v228, v229
	v_cvt_pknorm_i16_f32 v7, v230, v231
	v_pk_mul_f32 v[224:225], v[38:39], v[2:3] op_sel:[0,1] op_sel_hi:[1,1]
	v_pk_mul_f32 v[226:227], v[40:41], v[2:3] op_sel:[0,1] op_sel_hi:[1,1]
	v_cvt_pknorm_i16_f32 v8, v224, v225
	s_mov_b64 s[6:7], 0x1600
	v_cvt_pknorm_i16_f32 v9, v226, v227
	v_lshl_add_u64 v[10:11], v[4:5], 0, s[6:7]
	global_store_dwordx4 v[10:11], v[6:9], off sc0 sc1
	s_nop 1
	v_pk_mul_f32 v[6:7], v[12:13], s[4:5] op_sel_hi:[1,0]
	v_accvgpr_read_b32 v46, a104
	v_accvgpr_read_b32 v47, a105
	v_accvgpr_read_b32 v48, a106
	v_accvgpr_read_b32 v49, a107
	v_accvgpr_read_b32 v50, a108
	v_accvgpr_read_b32 v51, a109
	v_accvgpr_read_b32 v52, a110
	v_accvgpr_read_b32 v53, a111
	global_store_dwordx2 v0, v[6:7], s[2:3] offset:40
	v_mov_b64_e32 v[42:43], v[46:47]
	v_accvgpr_read_b32 v6, a248
	v_accvgpr_read_b32 v7, a232
	v_max3_f32 v8, |v42|, |v6|, |v7|
	v_accvgpr_read_b32 v9, a216
	v_accvgpr_read_b32 v14, a200
	v_max3_f32 v8, |v8|, |v9|, |v14|
	v_accvgpr_read_b32 v15, a184
	v_accvgpr_read_b32 v16, a168
	v_max3_f32 v8, |v8|, |v15|, |v16|
	v_accvgpr_read_b32 v10, a152
	v_accvgpr_read_b32 v17, a152
	v_max3_f32 v8, |v8|, |v17|, |v10|
	v_accvgpr_read_b32 v19, a249
	v_accvgpr_read_b32 v20, a233
	v_max3_f32 v10, |v43|, |v19|, |v20|
	v_accvgpr_read_b32 v21, a217
	v_accvgpr_read_b32 v22, a201
	v_max3_f32 v10, |v10|, |v21|, |v22|
	v_accvgpr_read_b32 v23, a185
	v_accvgpr_read_b32 v24, a169
	v_max3_f32 v10, |v10|, |v23|, |v24|
	v_mov_b64_e32 v[44:45], v[48:49]
	v_accvgpr_read_b32 v25, a153
	v_max3_f32 v11, |v10|, |v25|, |v25|
	v_accvgpr_read_b32 v27, a250
	v_accvgpr_read_b32 v28, a234
	v_max3_f32 v10, |v44|, |v27|, |v28|
	v_accvgpr_read_b32 v29, a218
	v_accvgpr_read_b32 v30, a202
	v_max3_f32 v10, |v10|, |v29|, |v30|
	v_accvgpr_read_b32 v31, a186
	v_accvgpr_read_b32 v32, a170
	v_max3_f32 v10, |v10|, |v31|, |v32|
	v_accvgpr_read_b32 v33, a154
	v_max3_f32 v12, |v10|, |v33|, |v33|
	v_accvgpr_read_b32 v35, a251
	v_accvgpr_read_b32 v36, a235
	v_max3_f32 v10, |v45|, |v35|, |v36|
	v_accvgpr_read_b32 v37, a219
	v_accvgpr_read_b32 v38, a203
	v_max3_f32 v10, |v10|, |v37|, |v38|
	v_accvgpr_read_b32 v39, a187
	v_accvgpr_read_b32 v40, a171
	v_max3_f32 v10, |v10|, |v39|, |v40|
	v_accvgpr_read_b32 v41, a155
	v_max3_f32 v13, |v10|, |v41|, |v41|
	v_mov_b32_e32 v3, v42
	s_nop 1
	v_max_f32_dpp v8, v8, v8 quad_perm:[1,0,3,2] row_mask:0xf bank_mask:0xf
	v_max_f32_dpp v11, v11, v11 quad_perm:[1,0,3,2] row_mask:0xf bank_mask:0xf
	v_max_f32_dpp v12, v12, v12 quad_perm:[1,0,3,2] row_mask:0xf bank_mask:0xf
	v_max_f32_dpp v13, v13, v13 quad_perm:[1,0,3,2] row_mask:0xf bank_mask:0xf
	v_max_f32_dpp v8, v8, v8 quad_perm:[2,3,0,1] row_mask:0xf bank_mask:0xf
	v_max_f32_dpp v11, v11, v11 quad_perm:[2,3,0,1] row_mask:0xf bank_mask:0xf
	v_max_f32_dpp v12, v12, v12 quad_perm:[2,3,0,1] row_mask:0xf bank_mask:0xf
	v_max_f32_dpp v13, v13, v13 quad_perm:[2,3,0,1] row_mask:0xf bank_mask:0xf
	v_max_f32_dpp v8, v8, v8 row_half_mirror row_mask:0xf bank_mask:0xf
	v_max_f32_dpp v11, v11, v11 row_half_mirror row_mask:0xf bank_mask:0xf
	v_max_f32_dpp v12, v12, v12 row_half_mirror row_mask:0xf bank_mask:0xf
	v_max_f32_dpp v13, v13, v13 row_half_mirror row_mask:0xf bank_mask:0xf
	v_max_f32_dpp v8, v8, v8 row_mirror row_mask:0xf bank_mask:0xf
	v_max_f32_dpp v11, v11, v11 row_mirror row_mask:0xf bank_mask:0xf
	v_max_f32_dpp v12, v12, v12 row_mirror row_mask:0xf bank_mask:0xf
	v_max_f32_dpp v13, v13, v13 row_mirror row_mask:0xf bank_mask:0xf
	s_nop 0
	ds_swizzle_b32 v232, v8 offset:swizzle(SWAP,16)
	ds_swizzle_b32 v233, v11 offset:swizzle(SWAP,16)
	ds_swizzle_b32 v234, v12 offset:swizzle(SWAP,16)
	ds_swizzle_b32 v235, v13 offset:swizzle(SWAP,16)
	s_waitcnt lgkmcnt(0)
	v_max_f32_e32 v10, v8, v232
	v_rcp_f32_e32 v8, v10
	v_cmp_lt_f32_e32 vcc, 0, v10
	s_waitcnt lgkmcnt(0)
	v_max_f32_e32 v11, v11, v233
	v_mov_b32_e32 v18, v43
	s_mov_b64 s[6:7], 0x2000
	v_cndmask_b32_e32 v42, 0, v8, vcc
	v_mul_f32_e32 v3, v42, v3
	v_mul_f32_e32 v6, v42, v6
	v_cvt_pknorm_i16_f32 v6, v3, v6
	v_mul_f32_e32 v3, v42, v7
	v_mul_f32_e32 v7, v42, v9
	v_cvt_pknorm_i16_f32 v7, v3, v7
	v_pk_mul_f32 v[228:229], v[14:15], v[42:43] op_sel_hi:[1,0]
	v_pk_mul_f32 v[230:231], v[16:17], v[42:43] op_sel_hi:[1,0]
	v_cvt_pknorm_i16_f32 v8, v228, v229
	v_cvt_pknorm_i16_f32 v9, v230, v231
	v_rcp_f32_e32 v3, v11
	v_cmp_lt_f32_e32 vcc, 0, v11
	v_lshl_add_u64 v[14:15], v[4:5], 0, s[6:7]
	global_store_dwordx4 v[14:15], v[6:9], off sc0 sc1
	v_cndmask_b32_e32 v3, 0, v3, vcc
	v_pk_mul_f32 v[224:225], v[18:19], v[2:3] op_sel:[0,1] op_sel_hi:[1,1]
	v_pk_mul_f32 v[226:227], v[20:21], v[2:3] op_sel:[0,1] op_sel_hi:[1,1]
	v_cvt_pknorm_i16_f32 v6, v224, v225
	v_cvt_pknorm_i16_f32 v7, v226, v227
	v_pk_mul_f32 v[228:229], v[22:23], v[2:3] op_sel:[0,1] op_sel_hi:[1,1]
	v_pk_mul_f32 v[230:231], v[24:25], v[2:3] op_sel:[0,1] op_sel_hi:[1,1]
	v_cvt_pknorm_i16_f32 v8, v228, v229
	s_waitcnt lgkmcnt(0)
	v_max_f32_e32 v12, v12, v234
	v_cvt_pknorm_i16_f32 v9, v230, v231
	v_rcp_f32_e32 v3, v12
	s_mov_b64 s[6:7], 0x2200
	v_cmp_lt_f32_e32 vcc, 0, v12
	v_mov_b32_e32 v26, v44
	v_lshl_add_u64 v[14:15], v[4:5], 0, s[6:7]
	global_store_dwordx4 v[14:15], v[6:9], off sc0 sc1
	s_nop 1
	v_pk_mul_f32 v[6:7], v[10:11], s[4:5] op_sel_hi:[1,0]
	v_cndmask_b32_e32 v3, 0, v3, vcc
	global_store_dwordx2 v0, v[6:7], s[2:3] offset:64
	v_pk_mul_f32 v[224:225], v[26:27], v[2:3] op_sel:[0,1] op_sel_hi:[1,1]
	v_pk_mul_f32 v[226:227], v[28:29], v[2:3] op_sel:[0,1] op_sel_hi:[1,1]
	v_cvt_pknorm_i16_f32 v6, v224, v225
	v_cvt_pknorm_i16_f32 v7, v226, v227
	v_pk_mul_f32 v[228:229], v[30:31], v[2:3] op_sel:[0,1] op_sel_hi:[1,1]
	v_pk_mul_f32 v[230:231], v[32:33], v[2:3] op_sel:[0,1] op_sel_hi:[1,1]
	v_cvt_pknorm_i16_f32 v8, v228, v229
	s_waitcnt lgkmcnt(0)
	v_max_f32_e32 v13, v13, v235
	v_cvt_pknorm_i16_f32 v9, v230, v231
	v_rcp_f32_e32 v3, v13
	v_cmp_lt_f32_e32 vcc, 0, v13
	v_mov_b32_e32 v34, v45
	s_mov_b64 s[6:7], 0x2400
	v_cndmask_b32_e32 v3, 0, v3, vcc
	v_lshl_add_u64 v[10:11], v[4:5], 0, s[6:7]
	global_store_dwordx4 v[10:11], v[6:9], off sc0 sc1
	v_pk_mul_f32 v[224:225], v[34:35], v[2:3] op_sel:[0,1] op_sel_hi:[1,1]
	v_pk_mul_f32 v[226:227], v[36:37], v[2:3] op_sel:[0,1] op_sel_hi:[1,1]
	v_cvt_pknorm_i16_f32 v6, v224, v225
	v_cvt_pknorm_i16_f32 v7, v226, v227
	v_pk_mul_f32 v[228:229], v[38:39], v[2:3] op_sel:[0,1] op_sel_hi:[1,1]
	v_pk_mul_f32 v[230:231], v[40:41], v[2:3] op_sel:[0,1] op_sel_hi:[1,1]
	v_cvt_pknorm_i16_f32 v8, v228, v229
	s_mov_b64 s[6:7], 0x2600
	v_cvt_pknorm_i16_f32 v9, v230, v231
	v_lshl_add_u64 v[10:11], v[4:5], 0, s[6:7]
	global_store_dwordx4 v[10:11], v[6:9], off sc0 sc1
	s_nop 1
	v_pk_mul_f32 v[6:7], v[12:13], s[4:5] op_sel_hi:[1,0]
	v_mov_b64_e32 v[46:47], v[50:51]
	v_mov_b64_e32 v[48:49], v[52:53]
	global_store_dwordx2 v0, v[6:7], s[2:3] offset:72
	v_mov_b64_e32 v[32:33], v[46:47]
	v_accvgpr_read_b32 v6, a252
	v_accvgpr_read_b32 v7, a236
	v_max3_f32 v8, |v32|, |v6|, |v7|
	v_accvgpr_read_b32 v9, a220
	v_accvgpr_read_b32 v14, a204
	v_max3_f32 v8, |v8|, |v9|, |v14|
	v_accvgpr_read_b32 v15, a188
	v_accvgpr_read_b32 v16, a172
	v_max3_f32 v8, |v8|, |v15|, |v16|
	v_accvgpr_read_b32 v10, a156
	v_accvgpr_read_b32 v17, a156
	v_max3_f32 v8, |v8|, |v17|, |v10|
	v_accvgpr_read_b32 v19, a253
	v_accvgpr_read_b32 v20, a237
	v_max3_f32 v10, |v33|, |v19|, |v20|
	v_accvgpr_read_b32 v21, a221
	v_accvgpr_read_b32 v22, a205
	v_max3_f32 v10, |v10|, |v21|, |v22|
	v_accvgpr_read_b32 v23, a189
	v_accvgpr_read_b32 v24, a173
	v_max3_f32 v10, |v10|, |v23|, |v24|
	v_mov_b64_e32 v[34:35], v[48:49]
	v_accvgpr_read_b32 v25, a157
	v_max3_f32 v11, |v10|, |v25|, |v25|
	v_accvgpr_read_b32 v27, a254
	v_accvgpr_read_b32 v28, a238
	v_max3_f32 v10, |v34|, |v27|, |v28|
	v_accvgpr_read_b32 v29, a222
	v_accvgpr_read_b32 v30, a206
	v_max3_f32 v10, |v10|, |v29|, |v30|
	v_mov_b32_e32 v3, v32
	v_accvgpr_read_b32 v31, a190
	v_accvgpr_read_b32 v32, a174
	v_max3_f32 v10, |v10|, |v31|, |v32|
	v_mov_b32_e32 v18, v33
	v_mov_b32_e32 v26, v34
	v_accvgpr_read_b32 v33, a158
	v_max3_f32 v12, |v10|, |v33|, |v33|
	v_mov_b32_e32 v34, v35
	v_accvgpr_read_b32 v35, a255
	v_accvgpr_read_b32 v36, a239
	v_max3_f32 v10, |v34|, |v35|, |v36|
	v_accvgpr_read_b32 v37, a223
	v_accvgpr_read_b32 v38, a207
	v_max3_f32 v10, |v10|, |v37|, |v38|
	v_accvgpr_read_b32 v39, a191
	v_accvgpr_read_b32 v40, a175
	v_max3_f32 v10, |v10|, |v39|, |v40|
	v_accvgpr_read_b32 v41, a159
	v_max3_f32 v13, |v10|, |v41|, |v41|
	s_mov_b64 s[6:7], 0x3000
	s_nop 1
	v_max_f32_dpp v8, v8, v8 quad_perm:[1,0,3,2] row_mask:0xf bank_mask:0xf
	v_max_f32_dpp v11, v11, v11 quad_perm:[1,0,3,2] row_mask:0xf bank_mask:0xf
	v_max_f32_dpp v12, v12, v12 quad_perm:[1,0,3,2] row_mask:0xf bank_mask:0xf
	v_max_f32_dpp v13, v13, v13 quad_perm:[1,0,3,2] row_mask:0xf bank_mask:0xf
	v_max_f32_dpp v8, v8, v8 quad_perm:[2,3,0,1] row_mask:0xf bank_mask:0xf
	v_max_f32_dpp v11, v11, v11 quad_perm:[2,3,0,1] row_mask:0xf bank_mask:0xf
	v_max_f32_dpp v12, v12, v12 quad_perm:[2,3,0,1] row_mask:0xf bank_mask:0xf
	v_max_f32_dpp v13, v13, v13 quad_perm:[2,3,0,1] row_mask:0xf bank_mask:0xf
	v_max_f32_dpp v8, v8, v8 row_half_mirror row_mask:0xf bank_mask:0xf
	v_max_f32_dpp v11, v11, v11 row_half_mirror row_mask:0xf bank_mask:0xf
	v_max_f32_dpp v12, v12, v12 row_half_mirror row_mask:0xf bank_mask:0xf
	v_max_f32_dpp v13, v13, v13 row_half_mirror row_mask:0xf bank_mask:0xf
	v_max_f32_dpp v8, v8, v8 row_mirror row_mask:0xf bank_mask:0xf
	v_max_f32_dpp v11, v11, v11 row_mirror row_mask:0xf bank_mask:0xf
	v_max_f32_dpp v12, v12, v12 row_mirror row_mask:0xf bank_mask:0xf
	v_max_f32_dpp v13, v13, v13 row_mirror row_mask:0xf bank_mask:0xf
	s_nop 0
	ds_swizzle_b32 v232, v8 offset:swizzle(SWAP,16)
	ds_swizzle_b32 v233, v11 offset:swizzle(SWAP,16)
	ds_swizzle_b32 v234, v12 offset:swizzle(SWAP,16)
	ds_swizzle_b32 v235, v13 offset:swizzle(SWAP,16)
	s_waitcnt lgkmcnt(0)
	v_max_f32_e32 v10, v8, v232
	v_rcp_f32_e32 v8, v10
	v_cmp_lt_f32_e32 vcc, 0, v10
	s_waitcnt lgkmcnt(0)
	v_max_f32_e32 v11, v11, v233
	s_waitcnt lgkmcnt(0)
	v_max_f32_e32 v12, v12, v234
	v_cndmask_b32_e32 v42, 0, v8, vcc
	v_mul_f32_e32 v3, v42, v3
	v_mul_f32_e32 v6, v42, v6
	v_cvt_pknorm_i16_f32 v6, v3, v6
	v_mul_f32_e32 v3, v42, v7
	v_mul_f32_e32 v7, v42, v9
	v_cvt_pknorm_i16_f32 v7, v3, v7
	v_pk_mul_f32 v[224:225], v[14:15], v[42:43] op_sel_hi:[1,0]
	v_pk_mul_f32 v[226:227], v[16:17], v[42:43] op_sel_hi:[1,0]
	v_cvt_pknorm_i16_f32 v8, v224, v225
	v_cvt_pknorm_i16_f32 v9, v226, v227
	v_rcp_f32_e32 v3, v11
	v_cmp_lt_f32_e32 vcc, 0, v11
	v_lshl_add_u64 v[14:15], v[4:5], 0, s[6:7]
	global_store_dwordx4 v[14:15], v[6:9], off sc0 sc1
	s_mov_b64 s[6:7], 0x3200
	v_cndmask_b32_e32 v3, 0, v3, vcc
	v_pk_mul_f32 v[228:229], v[18:19], v[2:3] op_sel:[0,1] op_sel_hi:[1,1]
	v_pk_mul_f32 v[230:231], v[20:21], v[2:3] op_sel:[0,1] op_sel_hi:[1,1]
	v_cvt_pknorm_i16_f32 v6, v228, v229
	v_cvt_pknorm_i16_f32 v7, v230, v231
	v_pk_mul_f32 v[224:225], v[22:23], v[2:3] op_sel:[0,1] op_sel_hi:[1,1]
	v_pk_mul_f32 v[226:227], v[24:25], v[2:3] op_sel:[0,1] op_sel_hi:[1,1]
	v_cvt_pknorm_i16_f32 v8, v224, v225
	v_cvt_pknorm_i16_f32 v9, v226, v227
	v_rcp_f32_e32 v3, v12
	v_cmp_lt_f32_e32 vcc, 0, v12
	v_lshl_add_u64 v[14:15], v[4:5], 0, s[6:7]
	global_store_dwordx4 v[14:15], v[6:9], off sc0 sc1
	s_nop 1
	v_pk_mul_f32 v[6:7], v[10:11], s[4:5] op_sel_hi:[1,0]
	v_cndmask_b32_e32 v3, 0, v3, vcc
	global_store_dwordx2 v0, v[6:7], s[2:3] offset:96
	v_pk_mul_f32 v[228:229], v[26:27], v[2:3] op_sel:[0,1] op_sel_hi:[1,1]
	v_pk_mul_f32 v[230:231], v[28:29], v[2:3] op_sel:[0,1] op_sel_hi:[1,1]
	v_cvt_pknorm_i16_f32 v6, v228, v229
	v_cvt_pknorm_i16_f32 v7, v230, v231
	v_pk_mul_f32 v[224:225], v[30:31], v[2:3] op_sel:[0,1] op_sel_hi:[1,1]
	v_pk_mul_f32 v[226:227], v[32:33], v[2:3] op_sel:[0,1] op_sel_hi:[1,1]
	v_cvt_pknorm_i16_f32 v8, v224, v225
	s_waitcnt lgkmcnt(0)
	v_max_f32_e32 v13, v13, v235
	v_cvt_pknorm_i16_f32 v9, v226, v227
	v_rcp_f32_e32 v3, v13
	v_cmp_lt_f32_e32 vcc, 0, v13
	s_mov_b64 s[6:7], 0x3400
	v_lshl_add_u64 v[10:11], v[4:5], 0, s[6:7]
	v_cndmask_b32_e32 v3, 0, v3, vcc
	global_store_dwordx4 v[10:11], v[6:9], off sc0 sc1
	v_pk_mul_f32 v[228:229], v[34:35], v[2:3] op_sel:[0,1] op_sel_hi:[1,1]
	v_pk_mul_f32 v[230:231], v[36:37], v[2:3] op_sel:[0,1] op_sel_hi:[1,1]
	v_cvt_pknorm_i16_f32 v6, v228, v229
	v_cvt_pknorm_i16_f32 v7, v230, v231
	v_pk_mul_f32 v[224:225], v[38:39], v[2:3] op_sel:[0,1] op_sel_hi:[1,1]
	v_pk_mul_f32 v[226:227], v[40:41], v[2:3] op_sel:[0,1] op_sel_hi:[1,1]
	v_cvt_pknorm_i16_f32 v8, v224, v225
	s_mov_b64 s[6:7], 0x3600
	v_cvt_pknorm_i16_f32 v9, v226, v227
	v_lshl_add_u64 v[10:11], v[4:5], 0, s[6:7]
	global_store_dwordx4 v[10:11], v[6:9], off sc0 sc1
	s_nop 1
	v_pk_mul_f32 v[6:7], v[12:13], s[4:5] op_sel_hi:[1,0]
	global_store_dwordx2 v0, v[6:7], s[2:3] offset:104
	v_accvgpr_read_b32 v3, a0
	v_accvgpr_read_b32 v6, a16
	v_accvgpr_read_b32 v7, a32
	v_max3_f32 v8, |v3|, |v6|, |v7|
	v_accvgpr_read_b32 v9, a48
	v_accvgpr_read_b32 v14, a64
	v_max3_f32 v8, |v8|, |v9|, |v14|
	v_accvgpr_read_b32 v15, a112
	v_accvgpr_read_b32 v16, a128
	v_max3_f32 v8, |v8|, |v15|, |v16|
	v_accvgpr_read_b32 v10, a80
	v_accvgpr_read_b32 v17, a80
	v_max3_f32 v8, |v8|, |v17|, |v10|
	v_accvgpr_read_b32 v18, a1
	v_accvgpr_read_b32 v19, a17
	v_accvgpr_read_b32 v20, a33
	v_max3_f32 v10, |v18|, |v19|, |v20|
	v_accvgpr_read_b32 v21, a49
	v_accvgpr_read_b32 v22, a65
	v_max3_f32 v10, |v10|, |v21|, |v22|
	v_accvgpr_read_b32 v23, a113
	v_accvgpr_read_b32 v24, a129
	v_max3_f32 v10, |v10|, |v23|, |v24|
	v_accvgpr_read_b32 v25, a81
	v_max3_f32 v11, |v10|, |v25|, |v25|
	v_accvgpr_read_b32 v26, a2
	v_accvgpr_read_b32 v27, a18
	v_accvgpr_read_b32 v28, a34
	v_max3_f32 v10, |v26|, |v27|, |v28|
	v_accvgpr_read_b32 v29, a50
	v_accvgpr_read_b32 v30, a66
	v_max3_f32 v10, |v10|, |v29|, |v30|
	v_accvgpr_read_b32 v31, a114
	v_accvgpr_read_b32 v32, a130
	v_max3_f32 v10, |v10|, |v31|, |v32|
	v_accvgpr_read_b32 v33, a82
	v_max3_f32 v12, |v10|, |v33|, |v33|
	v_accvgpr_read_b32 v34, a3
	v_accvgpr_read_b32 v35, a19
	v_accvgpr_read_b32 v36, a35
	v_max3_f32 v10, |v34|, |v35|, |v36|
	v_accvgpr_read_b32 v37, a51
	v_accvgpr_read_b32 v38, a67
	v_max3_f32 v10, |v10|, |v37|, |v38|
	v_accvgpr_read_b32 v39, a115
	v_accvgpr_read_b32 v40, a131
	v_max3_f32 v10, |v10|, |v39|, |v40|
	v_accvgpr_read_b32 v41, a83
	v_max3_f32 v13, |v10|, |v41|, |v41|
	s_mov_b64 s[6:7], 0x4000
	s_nop 1
	v_max_f32_dpp v8, v8, v8 quad_perm:[1,0,3,2] row_mask:0xf bank_mask:0xf
	v_max_f32_dpp v11, v11, v11 quad_perm:[1,0,3,2] row_mask:0xf bank_mask:0xf
	v_max_f32_dpp v12, v12, v12 quad_perm:[1,0,3,2] row_mask:0xf bank_mask:0xf
	v_max_f32_dpp v13, v13, v13 quad_perm:[1,0,3,2] row_mask:0xf bank_mask:0xf
	v_max_f32_dpp v8, v8, v8 quad_perm:[2,3,0,1] row_mask:0xf bank_mask:0xf
	v_max_f32_dpp v11, v11, v11 quad_perm:[2,3,0,1] row_mask:0xf bank_mask:0xf
	v_max_f32_dpp v12, v12, v12 quad_perm:[2,3,0,1] row_mask:0xf bank_mask:0xf
	v_max_f32_dpp v13, v13, v13 quad_perm:[2,3,0,1] row_mask:0xf bank_mask:0xf
	v_max_f32_dpp v8, v8, v8 row_half_mirror row_mask:0xf bank_mask:0xf
	v_max_f32_dpp v11, v11, v11 row_half_mirror row_mask:0xf bank_mask:0xf
	v_max_f32_dpp v12, v12, v12 row_half_mirror row_mask:0xf bank_mask:0xf
	v_max_f32_dpp v13, v13, v13 row_half_mirror row_mask:0xf bank_mask:0xf
	v_max_f32_dpp v8, v8, v8 row_mirror row_mask:0xf bank_mask:0xf
	v_max_f32_dpp v11, v11, v11 row_mirror row_mask:0xf bank_mask:0xf
	v_max_f32_dpp v12, v12, v12 row_mirror row_mask:0xf bank_mask:0xf
	v_max_f32_dpp v13, v13, v13 row_mirror row_mask:0xf bank_mask:0xf
	s_nop 0
	ds_swizzle_b32 v232, v8 offset:swizzle(SWAP,16)
	ds_swizzle_b32 v233, v11 offset:swizzle(SWAP,16)
	ds_swizzle_b32 v234, v12 offset:swizzle(SWAP,16)
	ds_swizzle_b32 v235, v13 offset:swizzle(SWAP,16)
	s_waitcnt lgkmcnt(0)
	v_max_f32_e32 v10, v8, v232
	v_rcp_f32_e32 v8, v10
	v_cmp_lt_f32_e32 vcc, 0, v10
	s_waitcnt lgkmcnt(0)
	v_max_f32_e32 v11, v11, v233
	s_waitcnt lgkmcnt(0)
	v_max_f32_e32 v12, v12, v234
	v_cndmask_b32_e32 v42, 0, v8, vcc
	v_mul_f32_e32 v3, v42, v3
	v_mul_f32_e32 v6, v42, v6
	v_cvt_pknorm_i16_f32 v6, v3, v6
	v_mul_f32_e32 v3, v42, v7
	v_mul_f32_e32 v7, v42, v9
	v_cvt_pknorm_i16_f32 v7, v3, v7
	v_pk_mul_f32 v[228:229], v[14:15], v[42:43] op_sel_hi:[1,0]
	v_pk_mul_f32 v[230:231], v[16:17], v[42:43] op_sel_hi:[1,0]
	v_cvt_pknorm_i16_f32 v8, v228, v229
	v_cvt_pknorm_i16_f32 v9, v230, v231
	v_rcp_f32_e32 v3, v11
	v_cmp_lt_f32_e32 vcc, 0, v11
	v_lshl_add_u64 v[14:15], v[4:5], 0, s[6:7]
	global_store_dwordx4 v[14:15], v[6:9], off sc0 sc1
	s_mov_b64 s[6:7], 0x4200
	v_cndmask_b32_e32 v3, 0, v3, vcc
	v_pk_mul_f32 v[224:225], v[18:19], v[2:3] op_sel:[0,1] op_sel_hi:[1,1]
	v_pk_mul_f32 v[226:227], v[20:21], v[2:3] op_sel:[0,1] op_sel_hi:[1,1]
	v_cvt_pknorm_i16_f32 v6, v224, v225
	v_cvt_pknorm_i16_f32 v7, v226, v227
	v_pk_mul_f32 v[228:229], v[22:23], v[2:3] op_sel:[0,1] op_sel_hi:[1,1]
	v_pk_mul_f32 v[230:231], v[24:25], v[2:3] op_sel:[0,1] op_sel_hi:[1,1]
	v_cvt_pknorm_i16_f32 v8, v228, v229
	v_cvt_pknorm_i16_f32 v9, v230, v231
	v_rcp_f32_e32 v3, v12
	v_cmp_lt_f32_e32 vcc, 0, v12
	v_lshl_add_u64 v[14:15], v[4:5], 0, s[6:7]
	global_store_dwordx4 v[14:15], v[6:9], off sc0 sc1
	s_nop 1
	v_pk_mul_f32 v[6:7], v[10:11], s[4:5] op_sel_hi:[1,0]
	v_cndmask_b32_e32 v3, 0, v3, vcc
	global_store_dwordx2 v0, v[6:7], s[2:3] offset:128
	v_pk_mul_f32 v[224:225], v[26:27], v[2:3] op_sel:[0,1] op_sel_hi:[1,1]
	v_pk_mul_f32 v[226:227], v[28:29], v[2:3] op_sel:[0,1] op_sel_hi:[1,1]
	v_cvt_pknorm_i16_f32 v6, v224, v225
	v_cvt_pknorm_i16_f32 v7, v226, v227
	v_pk_mul_f32 v[228:229], v[30:31], v[2:3] op_sel:[0,1] op_sel_hi:[1,1]
	v_pk_mul_f32 v[230:231], v[32:33], v[2:3] op_sel:[0,1] op_sel_hi:[1,1]
	v_cvt_pknorm_i16_f32 v8, v228, v229
	s_waitcnt lgkmcnt(0)
	v_max_f32_e32 v13, v13, v235
	v_cvt_pknorm_i16_f32 v9, v230, v231
	v_rcp_f32_e32 v3, v13
	v_cmp_lt_f32_e32 vcc, 0, v13
	s_mov_b64 s[6:7], 0x4400
	v_lshl_add_u64 v[10:11], v[4:5], 0, s[6:7]
	v_cndmask_b32_e32 v3, 0, v3, vcc
	global_store_dwordx4 v[10:11], v[6:9], off sc0 sc1
	v_pk_mul_f32 v[224:225], v[34:35], v[2:3] op_sel:[0,1] op_sel_hi:[1,1]
	v_pk_mul_f32 v[226:227], v[36:37], v[2:3] op_sel:[0,1] op_sel_hi:[1,1]
	v_cvt_pknorm_i16_f32 v6, v224, v225
	v_cvt_pknorm_i16_f32 v7, v226, v227
	v_pk_mul_f32 v[228:229], v[38:39], v[2:3] op_sel:[0,1] op_sel_hi:[1,1]
	v_pk_mul_f32 v[230:231], v[40:41], v[2:3] op_sel:[0,1] op_sel_hi:[1,1]
	v_cvt_pknorm_i16_f32 v8, v228, v229
	s_mov_b64 s[6:7], 0x4600
	v_cvt_pknorm_i16_f32 v9, v230, v231
	v_lshl_add_u64 v[10:11], v[4:5], 0, s[6:7]
	global_store_dwordx4 v[10:11], v[6:9], off sc0 sc1
	s_nop 1
	v_pk_mul_f32 v[6:7], v[12:13], s[4:5] op_sel_hi:[1,0]
	global_store_dwordx2 v0, v[6:7], s[2:3] offset:136
	v_accvgpr_read_b32 v3, a4
	v_accvgpr_read_b32 v6, a20
	v_accvgpr_read_b32 v7, a36
	v_max3_f32 v8, |v3|, |v6|, |v7|
	v_accvgpr_read_b32 v9, a52
	v_accvgpr_read_b32 v14, a68
	v_max3_f32 v8, |v8|, |v9|, |v14|
	v_accvgpr_read_b32 v15, a116
	v_accvgpr_read_b32 v16, a132
	v_max3_f32 v8, |v8|, |v15|, |v16|
	v_accvgpr_read_b32 v10, a84
	v_accvgpr_read_b32 v17, a84
	v_max3_f32 v8, |v8|, |v17|, |v10|
	v_accvgpr_read_b32 v18, a5
	v_accvgpr_read_b32 v19, a21
	v_accvgpr_read_b32 v20, a37
	v_max3_f32 v10, |v18|, |v19|, |v20|
	v_accvgpr_read_b32 v21, a53
	v_accvgpr_read_b32 v22, a69
	v_max3_f32 v10, |v10|, |v21|, |v22|
	v_accvgpr_read_b32 v23, a117
	v_accvgpr_read_b32 v24, a133
	v_max3_f32 v10, |v10|, |v23|, |v24|
	v_accvgpr_read_b32 v25, a85
	v_max3_f32 v11, |v10|, |v25|, |v25|
	v_accvgpr_read_b32 v26, a6
	v_accvgpr_read_b32 v27, a22
	v_accvgpr_read_b32 v28, a38
	v_max3_f32 v10, |v26|, |v27|, |v28|
	v_accvgpr_read_b32 v29, a54
	v_accvgpr_read_b32 v30, a70
	v_max3_f32 v10, |v10|, |v29|, |v30|
	v_accvgpr_read_b32 v31, a118
	v_accvgpr_read_b32 v32, a134
	v_max3_f32 v10, |v10|, |v31|, |v32|
	v_accvgpr_read_b32 v33, a86
	v_max3_f32 v12, |v10|, |v33|, |v33|
	v_accvgpr_read_b32 v34, a7
	v_accvgpr_read_b32 v35, a23
	v_accvgpr_read_b32 v36, a39
	v_max3_f32 v10, |v34|, |v35|, |v36|
	v_accvgpr_read_b32 v37, a55
	v_accvgpr_read_b32 v38, a71
	v_max3_f32 v10, |v10|, |v37|, |v38|
	v_accvgpr_read_b32 v39, a119
	v_accvgpr_read_b32 v40, a135
	v_max3_f32 v10, |v10|, |v39|, |v40|
	v_accvgpr_read_b32 v41, a87
	v_max3_f32 v13, |v10|, |v41|, |v41|
	s_mov_b64 s[6:7], 0x5000
	s_nop 1
	v_max_f32_dpp v8, v8, v8 quad_perm:[1,0,3,2] row_mask:0xf bank_mask:0xf
	v_max_f32_dpp v11, v11, v11 quad_perm:[1,0,3,2] row_mask:0xf bank_mask:0xf
	v_max_f32_dpp v12, v12, v12 quad_perm:[1,0,3,2] row_mask:0xf bank_mask:0xf
	v_max_f32_dpp v13, v13, v13 quad_perm:[1,0,3,2] row_mask:0xf bank_mask:0xf
	v_max_f32_dpp v8, v8, v8 quad_perm:[2,3,0,1] row_mask:0xf bank_mask:0xf
	v_max_f32_dpp v11, v11, v11 quad_perm:[2,3,0,1] row_mask:0xf bank_mask:0xf
	v_max_f32_dpp v12, v12, v12 quad_perm:[2,3,0,1] row_mask:0xf bank_mask:0xf
	v_max_f32_dpp v13, v13, v13 quad_perm:[2,3,0,1] row_mask:0xf bank_mask:0xf
	v_max_f32_dpp v8, v8, v8 row_half_mirror row_mask:0xf bank_mask:0xf
	v_max_f32_dpp v11, v11, v11 row_half_mirror row_mask:0xf bank_mask:0xf
	v_max_f32_dpp v12, v12, v12 row_half_mirror row_mask:0xf bank_mask:0xf
	v_max_f32_dpp v13, v13, v13 row_half_mirror row_mask:0xf bank_mask:0xf
	v_max_f32_dpp v8, v8, v8 row_mirror row_mask:0xf bank_mask:0xf
	v_max_f32_dpp v11, v11, v11 row_mirror row_mask:0xf bank_mask:0xf
	v_max_f32_dpp v12, v12, v12 row_mirror row_mask:0xf bank_mask:0xf
	v_max_f32_dpp v13, v13, v13 row_mirror row_mask:0xf bank_mask:0xf
	s_nop 0
	ds_swizzle_b32 v232, v8 offset:swizzle(SWAP,16)
	ds_swizzle_b32 v233, v11 offset:swizzle(SWAP,16)
	ds_swizzle_b32 v234, v12 offset:swizzle(SWAP,16)
	ds_swizzle_b32 v235, v13 offset:swizzle(SWAP,16)
	s_waitcnt lgkmcnt(0)
	v_max_f32_e32 v10, v8, v232
	v_rcp_f32_e32 v8, v10
	v_cmp_lt_f32_e32 vcc, 0, v10
	s_waitcnt lgkmcnt(0)
	v_max_f32_e32 v11, v11, v233
	s_waitcnt lgkmcnt(0)
	v_max_f32_e32 v12, v12, v234
	v_cndmask_b32_e32 v42, 0, v8, vcc
	v_mul_f32_e32 v3, v42, v3
	v_mul_f32_e32 v6, v42, v6
	v_cvt_pknorm_i16_f32 v6, v3, v6
	v_mul_f32_e32 v3, v42, v7
	v_mul_f32_e32 v7, v42, v9
	v_cvt_pknorm_i16_f32 v7, v3, v7
	v_pk_mul_f32 v[224:225], v[14:15], v[42:43] op_sel_hi:[1,0]
	v_pk_mul_f32 v[226:227], v[16:17], v[42:43] op_sel_hi:[1,0]
	v_cvt_pknorm_i16_f32 v8, v224, v225
	v_cvt_pknorm_i16_f32 v9, v226, v227
	v_rcp_f32_e32 v3, v11
	v_cmp_lt_f32_e32 vcc, 0, v11
	v_lshl_add_u64 v[14:15], v[4:5], 0, s[6:7]
	global_store_dwordx4 v[14:15], v[6:9], off sc0 sc1
	s_mov_b64 s[6:7], 0x5200
	v_cndmask_b32_e32 v3, 0, v3, vcc
	v_pk_mul_f32 v[228:229], v[18:19], v[2:3] op_sel:[0,1] op_sel_hi:[1,1]
	v_pk_mul_f32 v[230:231], v[20:21], v[2:3] op_sel:[0,1] op_sel_hi:[1,1]
	v_cvt_pknorm_i16_f32 v6, v228, v229
	v_cvt_pknorm_i16_f32 v7, v230, v231
	v_pk_mul_f32 v[224:225], v[22:23], v[2:3] op_sel:[0,1] op_sel_hi:[1,1]
	v_pk_mul_f32 v[226:227], v[24:25], v[2:3] op_sel:[0,1] op_sel_hi:[1,1]
	v_cvt_pknorm_i16_f32 v8, v224, v225
	v_cvt_pknorm_i16_f32 v9, v226, v227
	v_rcp_f32_e32 v3, v12
	v_cmp_lt_f32_e32 vcc, 0, v12
	v_lshl_add_u64 v[14:15], v[4:5], 0, s[6:7]
	global_store_dwordx4 v[14:15], v[6:9], off sc0 sc1
	s_nop 1
	v_pk_mul_f32 v[6:7], v[10:11], s[4:5] op_sel_hi:[1,0]
	v_cndmask_b32_e32 v3, 0, v3, vcc
	global_store_dwordx2 v0, v[6:7], s[2:3] offset:160
	v_pk_mul_f32 v[228:229], v[26:27], v[2:3] op_sel:[0,1] op_sel_hi:[1,1]
	v_pk_mul_f32 v[230:231], v[28:29], v[2:3] op_sel:[0,1] op_sel_hi:[1,1]
	v_cvt_pknorm_i16_f32 v6, v228, v229
	v_cvt_pknorm_i16_f32 v7, v230, v231
	v_pk_mul_f32 v[224:225], v[30:31], v[2:3] op_sel:[0,1] op_sel_hi:[1,1]
	v_pk_mul_f32 v[226:227], v[32:33], v[2:3] op_sel:[0,1] op_sel_hi:[1,1]
	v_cvt_pknorm_i16_f32 v8, v224, v225
	s_waitcnt lgkmcnt(0)
	v_max_f32_e32 v13, v13, v235
	v_cvt_pknorm_i16_f32 v9, v226, v227
	v_rcp_f32_e32 v3, v13
	v_cmp_lt_f32_e32 vcc, 0, v13
	s_mov_b64 s[6:7], 0x5400
	v_lshl_add_u64 v[10:11], v[4:5], 0, s[6:7]
	v_cndmask_b32_e32 v3, 0, v3, vcc
	global_store_dwordx4 v[10:11], v[6:9], off sc0 sc1
	v_pk_mul_f32 v[228:229], v[34:35], v[2:3] op_sel:[0,1] op_sel_hi:[1,1]
	v_pk_mul_f32 v[230:231], v[36:37], v[2:3] op_sel:[0,1] op_sel_hi:[1,1]
	v_cvt_pknorm_i16_f32 v6, v228, v229
	v_cvt_pknorm_i16_f32 v7, v230, v231
	v_pk_mul_f32 v[224:225], v[38:39], v[2:3] op_sel:[0,1] op_sel_hi:[1,1]
	v_pk_mul_f32 v[226:227], v[40:41], v[2:3] op_sel:[0,1] op_sel_hi:[1,1]
	v_cvt_pknorm_i16_f32 v8, v224, v225
	s_mov_b64 s[6:7], 0x5600
	v_cvt_pknorm_i16_f32 v9, v226, v227
	v_lshl_add_u64 v[10:11], v[4:5], 0, s[6:7]
	global_store_dwordx4 v[10:11], v[6:9], off sc0 sc1
	s_nop 1
	v_pk_mul_f32 v[6:7], v[12:13], s[4:5] op_sel_hi:[1,0]
	global_store_dwordx2 v0, v[6:7], s[2:3] offset:168
	v_accvgpr_read_b32 v3, a8
	v_accvgpr_read_b32 v6, a24
	v_accvgpr_read_b32 v7, a40
	v_max3_f32 v8, |v3|, |v6|, |v7|
	v_accvgpr_read_b32 v9, a56
	v_accvgpr_read_b32 v14, a72
	v_max3_f32 v8, |v8|, |v9|, |v14|
	v_accvgpr_read_b32 v15, a120
	v_accvgpr_read_b32 v16, a136
	v_max3_f32 v8, |v8|, |v15|, |v16|
	v_accvgpr_read_b32 v10, a88
	v_accvgpr_read_b32 v17, a88
	v_max3_f32 v8, |v8|, |v17|, |v10|
	v_accvgpr_read_b32 v18, a9
	v_accvgpr_read_b32 v19, a25
	v_accvgpr_read_b32 v20, a41
	v_max3_f32 v10, |v18|, |v19|, |v20|
	v_accvgpr_read_b32 v21, a57
	v_accvgpr_read_b32 v22, a73
	v_max3_f32 v10, |v10|, |v21|, |v22|
	v_accvgpr_read_b32 v23, a121
	v_accvgpr_read_b32 v24, a137
	v_max3_f32 v10, |v10|, |v23|, |v24|
	v_accvgpr_read_b32 v25, a89
	v_max3_f32 v11, |v10|, |v25|, |v25|
	v_accvgpr_read_b32 v26, a10
	v_accvgpr_read_b32 v27, a26
	v_accvgpr_read_b32 v28, a42
	v_max3_f32 v10, |v26|, |v27|, |v28|
	v_accvgpr_read_b32 v29, a58
	v_accvgpr_read_b32 v30, a74
	v_max3_f32 v10, |v10|, |v29|, |v30|
	v_accvgpr_read_b32 v31, a122
	v_accvgpr_read_b32 v32, a138
	v_max3_f32 v10, |v10|, |v31|, |v32|
	v_accvgpr_read_b32 v33, a90
	v_max3_f32 v12, |v10|, |v33|, |v33|
	v_accvgpr_read_b32 v34, a11
	v_accvgpr_read_b32 v35, a27
	v_accvgpr_read_b32 v36, a43
	v_max3_f32 v10, |v34|, |v35|, |v36|
	v_accvgpr_read_b32 v37, a59
	v_accvgpr_read_b32 v38, a75
	v_max3_f32 v10, |v10|, |v37|, |v38|
	v_accvgpr_read_b32 v39, a123
	v_accvgpr_read_b32 v40, a139
	v_max3_f32 v10, |v10|, |v39|, |v40|
	v_accvgpr_read_b32 v41, a91
	v_max3_f32 v13, |v10|, |v41|, |v41|
	s_mov_b64 s[6:7], 0x6000
	s_nop 1
	v_max_f32_dpp v8, v8, v8 quad_perm:[1,0,3,2] row_mask:0xf bank_mask:0xf
	v_max_f32_dpp v11, v11, v11 quad_perm:[1,0,3,2] row_mask:0xf bank_mask:0xf
	v_max_f32_dpp v12, v12, v12 quad_perm:[1,0,3,2] row_mask:0xf bank_mask:0xf
	v_max_f32_dpp v13, v13, v13 quad_perm:[1,0,3,2] row_mask:0xf bank_mask:0xf
	v_max_f32_dpp v8, v8, v8 quad_perm:[2,3,0,1] row_mask:0xf bank_mask:0xf
	v_max_f32_dpp v11, v11, v11 quad_perm:[2,3,0,1] row_mask:0xf bank_mask:0xf
	v_max_f32_dpp v12, v12, v12 quad_perm:[2,3,0,1] row_mask:0xf bank_mask:0xf
	v_max_f32_dpp v13, v13, v13 quad_perm:[2,3,0,1] row_mask:0xf bank_mask:0xf
	v_max_f32_dpp v8, v8, v8 row_half_mirror row_mask:0xf bank_mask:0xf
	v_max_f32_dpp v11, v11, v11 row_half_mirror row_mask:0xf bank_mask:0xf
	v_max_f32_dpp v12, v12, v12 row_half_mirror row_mask:0xf bank_mask:0xf
	v_max_f32_dpp v13, v13, v13 row_half_mirror row_mask:0xf bank_mask:0xf
	v_max_f32_dpp v8, v8, v8 row_mirror row_mask:0xf bank_mask:0xf
	v_max_f32_dpp v11, v11, v11 row_mirror row_mask:0xf bank_mask:0xf
	v_max_f32_dpp v12, v12, v12 row_mirror row_mask:0xf bank_mask:0xf
	v_max_f32_dpp v13, v13, v13 row_mirror row_mask:0xf bank_mask:0xf
	s_nop 0
	ds_swizzle_b32 v232, v8 offset:swizzle(SWAP,16)
	ds_swizzle_b32 v233, v11 offset:swizzle(SWAP,16)
	ds_swizzle_b32 v234, v12 offset:swizzle(SWAP,16)
	ds_swizzle_b32 v235, v13 offset:swizzle(SWAP,16)
	s_waitcnt lgkmcnt(0)
	v_max_f32_e32 v10, v8, v232
	v_rcp_f32_e32 v8, v10
	v_cmp_lt_f32_e32 vcc, 0, v10
	s_waitcnt lgkmcnt(0)
	v_max_f32_e32 v11, v11, v233
	s_waitcnt lgkmcnt(0)
	v_max_f32_e32 v12, v12, v234
	v_cndmask_b32_e32 v42, 0, v8, vcc
	v_mul_f32_e32 v3, v42, v3
	v_mul_f32_e32 v6, v42, v6
	v_cvt_pknorm_i16_f32 v6, v3, v6
	v_mul_f32_e32 v3, v42, v7
	v_mul_f32_e32 v7, v42, v9
	v_cvt_pknorm_i16_f32 v7, v3, v7
	v_pk_mul_f32 v[228:229], v[14:15], v[42:43] op_sel_hi:[1,0]
	v_pk_mul_f32 v[230:231], v[16:17], v[42:43] op_sel_hi:[1,0]
	v_cvt_pknorm_i16_f32 v8, v228, v229
	v_cvt_pknorm_i16_f32 v9, v230, v231
	v_rcp_f32_e32 v3, v11
	v_cmp_lt_f32_e32 vcc, 0, v11
	v_lshl_add_u64 v[14:15], v[4:5], 0, s[6:7]
	global_store_dwordx4 v[14:15], v[6:9], off sc0 sc1
	s_mov_b64 s[6:7], 0x6200
	v_cndmask_b32_e32 v3, 0, v3, vcc
	v_pk_mul_f32 v[224:225], v[18:19], v[2:3] op_sel:[0,1] op_sel_hi:[1,1]
	v_pk_mul_f32 v[226:227], v[20:21], v[2:3] op_sel:[0,1] op_sel_hi:[1,1]
	v_cvt_pknorm_i16_f32 v6, v224, v225
	v_cvt_pknorm_i16_f32 v7, v226, v227
	v_pk_mul_f32 v[228:229], v[22:23], v[2:3] op_sel:[0,1] op_sel_hi:[1,1]
	v_pk_mul_f32 v[230:231], v[24:25], v[2:3] op_sel:[0,1] op_sel_hi:[1,1]
	v_cvt_pknorm_i16_f32 v8, v228, v229
	v_cvt_pknorm_i16_f32 v9, v230, v231
	v_rcp_f32_e32 v3, v12
	v_cmp_lt_f32_e32 vcc, 0, v12
	v_lshl_add_u64 v[14:15], v[4:5], 0, s[6:7]
	global_store_dwordx4 v[14:15], v[6:9], off sc0 sc1
	s_nop 1
	v_pk_mul_f32 v[6:7], v[10:11], s[4:5] op_sel_hi:[1,0]
	v_cndmask_b32_e32 v3, 0, v3, vcc
	global_store_dwordx2 v0, v[6:7], s[2:3] offset:192
	v_pk_mul_f32 v[224:225], v[26:27], v[2:3] op_sel:[0,1] op_sel_hi:[1,1]
	v_pk_mul_f32 v[226:227], v[28:29], v[2:3] op_sel:[0,1] op_sel_hi:[1,1]
	v_cvt_pknorm_i16_f32 v6, v224, v225
	v_cvt_pknorm_i16_f32 v7, v226, v227
	v_pk_mul_f32 v[228:229], v[30:31], v[2:3] op_sel:[0,1] op_sel_hi:[1,1]
	v_pk_mul_f32 v[230:231], v[32:33], v[2:3] op_sel:[0,1] op_sel_hi:[1,1]
	v_cvt_pknorm_i16_f32 v8, v228, v229
	s_waitcnt lgkmcnt(0)
	v_max_f32_e32 v13, v13, v235
	v_cvt_pknorm_i16_f32 v9, v230, v231
	v_rcp_f32_e32 v3, v13
	v_cmp_lt_f32_e32 vcc, 0, v13
	s_mov_b64 s[6:7], 0x6400
	v_lshl_add_u64 v[10:11], v[4:5], 0, s[6:7]
	v_cndmask_b32_e32 v3, 0, v3, vcc
	global_store_dwordx4 v[10:11], v[6:9], off sc0 sc1
	v_pk_mul_f32 v[224:225], v[34:35], v[2:3] op_sel:[0,1] op_sel_hi:[1,1]
	v_pk_mul_f32 v[226:227], v[36:37], v[2:3] op_sel:[0,1] op_sel_hi:[1,1]
	v_cvt_pknorm_i16_f32 v6, v224, v225
	v_cvt_pknorm_i16_f32 v7, v226, v227
	v_pk_mul_f32 v[228:229], v[38:39], v[2:3] op_sel:[0,1] op_sel_hi:[1,1]
	v_pk_mul_f32 v[230:231], v[40:41], v[2:3] op_sel:[0,1] op_sel_hi:[1,1]
	v_cvt_pknorm_i16_f32 v8, v228, v229
	s_mov_b64 s[6:7], 0x6600
	v_cvt_pknorm_i16_f32 v9, v230, v231
	v_lshl_add_u64 v[10:11], v[4:5], 0, s[6:7]
	global_store_dwordx4 v[10:11], v[6:9], off sc0 sc1
	s_nop 1
	v_pk_mul_f32 v[6:7], v[12:13], s[4:5] op_sel_hi:[1,0]
	global_store_dwordx2 v0, v[6:7], s[2:3] offset:200
	v_accvgpr_read_b32 v3, a12
	v_accvgpr_read_b32 v6, a28
	v_accvgpr_read_b32 v7, a44
	v_max3_f32 v8, |v3|, |v6|, |v7|
	v_accvgpr_read_b32 v9, a60
	v_accvgpr_read_b32 v14, a76
	v_max3_f32 v8, |v8|, |v9|, |v14|
	v_accvgpr_read_b32 v15, a124
	v_accvgpr_read_b32 v16, a140
	v_max3_f32 v8, |v8|, |v15|, |v16|
	v_accvgpr_read_b32 v10, a92
	v_accvgpr_read_b32 v17, a92
	v_max3_f32 v8, |v8|, |v17|, |v10|
	v_accvgpr_read_b32 v18, a13
	v_accvgpr_read_b32 v19, a29
	v_accvgpr_read_b32 v20, a45
	v_max3_f32 v10, |v18|, |v19|, |v20|
	v_accvgpr_read_b32 v21, a61
	v_accvgpr_read_b32 v22, a77
	v_max3_f32 v10, |v10|, |v21|, |v22|
	v_accvgpr_read_b32 v23, a125
	v_accvgpr_read_b32 v24, a141
	v_max3_f32 v10, |v10|, |v23|, |v24|
	v_accvgpr_read_b32 v25, a93
	v_max3_f32 v11, |v10|, |v25|, |v25|
	v_accvgpr_read_b32 v26, a14
	v_accvgpr_read_b32 v27, a30
	v_accvgpr_read_b32 v28, a46
	v_max3_f32 v10, |v26|, |v27|, |v28|
	v_accvgpr_read_b32 v29, a62
	v_accvgpr_read_b32 v30, a78
	v_max3_f32 v10, |v10|, |v29|, |v30|
	v_accvgpr_read_b32 v31, a126
	v_accvgpr_read_b32 v32, a142
	v_max3_f32 v10, |v10|, |v31|, |v32|
	v_accvgpr_read_b32 v33, a94
	v_max3_f32 v12, |v10|, |v33|, |v33|
	v_accvgpr_read_b32 v34, a15
	v_accvgpr_read_b32 v35, a31
	v_accvgpr_read_b32 v36, a47
	v_max3_f32 v10, |v34|, |v35|, |v36|
	v_accvgpr_read_b32 v37, a63
	v_accvgpr_read_b32 v38, a79
	v_max3_f32 v10, |v10|, |v37|, |v38|
	v_accvgpr_read_b32 v39, a127
	v_accvgpr_read_b32 v40, a143
	v_max3_f32 v10, |v10|, |v39|, |v40|
	v_accvgpr_read_b32 v41, a95
	v_max3_f32 v13, |v10|, |v41|, |v41|
	s_mov_b64 s[6:7], 0x7000
	s_nop 1
	v_max_f32_dpp v8, v8, v8 quad_perm:[1,0,3,2] row_mask:0xf bank_mask:0xf
	v_max_f32_dpp v11, v11, v11 quad_perm:[1,0,3,2] row_mask:0xf bank_mask:0xf
	v_max_f32_dpp v12, v12, v12 quad_perm:[1,0,3,2] row_mask:0xf bank_mask:0xf
	v_max_f32_dpp v13, v13, v13 quad_perm:[1,0,3,2] row_mask:0xf bank_mask:0xf
	v_max_f32_dpp v8, v8, v8 quad_perm:[2,3,0,1] row_mask:0xf bank_mask:0xf
	v_max_f32_dpp v11, v11, v11 quad_perm:[2,3,0,1] row_mask:0xf bank_mask:0xf
	v_max_f32_dpp v12, v12, v12 quad_perm:[2,3,0,1] row_mask:0xf bank_mask:0xf
	v_max_f32_dpp v13, v13, v13 quad_perm:[2,3,0,1] row_mask:0xf bank_mask:0xf
	v_max_f32_dpp v8, v8, v8 row_half_mirror row_mask:0xf bank_mask:0xf
	v_max_f32_dpp v11, v11, v11 row_half_mirror row_mask:0xf bank_mask:0xf
	v_max_f32_dpp v12, v12, v12 row_half_mirror row_mask:0xf bank_mask:0xf
	v_max_f32_dpp v13, v13, v13 row_half_mirror row_mask:0xf bank_mask:0xf
	v_max_f32_dpp v8, v8, v8 row_mirror row_mask:0xf bank_mask:0xf
	v_max_f32_dpp v11, v11, v11 row_mirror row_mask:0xf bank_mask:0xf
	v_max_f32_dpp v12, v12, v12 row_mirror row_mask:0xf bank_mask:0xf
	v_max_f32_dpp v13, v13, v13 row_mirror row_mask:0xf bank_mask:0xf
	s_nop 0
	ds_swizzle_b32 v232, v8 offset:swizzle(SWAP,16)
	ds_swizzle_b32 v233, v11 offset:swizzle(SWAP,16)
	ds_swizzle_b32 v234, v12 offset:swizzle(SWAP,16)
	ds_swizzle_b32 v235, v13 offset:swizzle(SWAP,16)
	s_waitcnt lgkmcnt(0)
	v_max_f32_e32 v10, v8, v232
	v_rcp_f32_e32 v8, v10
	v_cmp_lt_f32_e32 vcc, 0, v10
	s_waitcnt lgkmcnt(0)
	v_max_f32_e32 v11, v11, v233
	s_waitcnt lgkmcnt(0)
	v_max_f32_e32 v12, v12, v234
	v_cndmask_b32_e32 v42, 0, v8, vcc
	v_mul_f32_e32 v3, v42, v3
	v_mul_f32_e32 v6, v42, v6
	v_cvt_pknorm_i16_f32 v6, v3, v6
	v_mul_f32_e32 v3, v42, v7
	v_mul_f32_e32 v7, v42, v9
	v_cvt_pknorm_i16_f32 v7, v3, v7
	v_pk_mul_f32 v[224:225], v[14:15], v[42:43] op_sel_hi:[1,0]
	v_pk_mul_f32 v[226:227], v[16:17], v[42:43] op_sel_hi:[1,0]
	v_cvt_pknorm_i16_f32 v8, v224, v225
	v_cvt_pknorm_i16_f32 v9, v226, v227
	v_rcp_f32_e32 v3, v11
	v_cmp_lt_f32_e32 vcc, 0, v11
	v_lshl_add_u64 v[14:15], v[4:5], 0, s[6:7]
	global_store_dwordx4 v[14:15], v[6:9], off sc0 sc1
	s_mov_b64 s[6:7], 0x7200
	v_cndmask_b32_e32 v3, 0, v3, vcc
	v_pk_mul_f32 v[228:229], v[18:19], v[2:3] op_sel:[0,1] op_sel_hi:[1,1]
	v_pk_mul_f32 v[230:231], v[20:21], v[2:3] op_sel:[0,1] op_sel_hi:[1,1]
	v_cvt_pknorm_i16_f32 v6, v228, v229
	v_cvt_pknorm_i16_f32 v7, v230, v231
	v_pk_mul_f32 v[224:225], v[22:23], v[2:3] op_sel:[0,1] op_sel_hi:[1,1]
	v_pk_mul_f32 v[226:227], v[24:25], v[2:3] op_sel:[0,1] op_sel_hi:[1,1]
	v_cvt_pknorm_i16_f32 v8, v224, v225
	v_cvt_pknorm_i16_f32 v9, v226, v227
	v_rcp_f32_e32 v3, v12
	v_cmp_lt_f32_e32 vcc, 0, v12
	v_lshl_add_u64 v[14:15], v[4:5], 0, s[6:7]
	global_store_dwordx4 v[14:15], v[6:9], off sc0 sc1
	s_nop 1
	v_pk_mul_f32 v[6:7], v[10:11], s[4:5] op_sel_hi:[1,0]
	v_cndmask_b32_e32 v3, 0, v3, vcc
	global_store_dwordx2 v0, v[6:7], s[2:3] offset:224
	v_pk_mul_f32 v[228:229], v[26:27], v[2:3] op_sel:[0,1] op_sel_hi:[1,1]
	v_pk_mul_f32 v[230:231], v[28:29], v[2:3] op_sel:[0,1] op_sel_hi:[1,1]
	v_cvt_pknorm_i16_f32 v6, v228, v229
	v_cvt_pknorm_i16_f32 v7, v230, v231
	v_pk_mul_f32 v[224:225], v[30:31], v[2:3] op_sel:[0,1] op_sel_hi:[1,1]
	v_pk_mul_f32 v[226:227], v[32:33], v[2:3] op_sel:[0,1] op_sel_hi:[1,1]
	v_cvt_pknorm_i16_f32 v8, v224, v225
	s_waitcnt lgkmcnt(0)
	v_max_f32_e32 v13, v13, v235
	v_cvt_pknorm_i16_f32 v9, v226, v227
	v_rcp_f32_e32 v3, v13
	v_cmp_lt_f32_e32 vcc, 0, v13
	s_mov_b64 s[6:7], 0x7400
	v_lshl_add_u64 v[10:11], v[4:5], 0, s[6:7]
	v_cndmask_b32_e32 v3, 0, v3, vcc
	global_store_dwordx4 v[10:11], v[6:9], off sc0 sc1
	v_pk_mul_f32 v[228:229], v[34:35], v[2:3] op_sel:[0,1] op_sel_hi:[1,1]
	v_pk_mul_f32 v[230:231], v[36:37], v[2:3] op_sel:[0,1] op_sel_hi:[1,1]
	v_cvt_pknorm_i16_f32 v6, v228, v229
	v_cvt_pknorm_i16_f32 v7, v230, v231
	v_pk_mul_f32 v[224:225], v[38:39], v[2:3] op_sel:[0,1] op_sel_hi:[1,1]
	v_pk_mul_f32 v[226:227], v[40:41], v[2:3] op_sel:[0,1] op_sel_hi:[1,1]
	v_cvt_pknorm_i16_f32 v8, v224, v225
	s_mov_b64 s[6:7], 0x7600
	v_cvt_pknorm_i16_f32 v9, v226, v227
	v_lshl_add_u64 v[4:5], v[4:5], 0, s[6:7]
	global_store_dwordx4 v[4:5], v[6:9], off sc0 sc1
	v_pk_mul_f32 v[4:5], v[12:13], s[4:5] op_sel_hi:[1,0]
	global_store_dwordx2 v0, v[4:5], s[2:3] offset:232
	ds_bpermute_b32 v4, v133, v134
	s_lshl_b64 s[0:1], s[0:1], 2
	s_add_u32 s0, s26, s0
	s_addc_u32 s1, s27, s1
	v_mov_b32_e32 v3, v1
	v_cmp_gt_i32_e32 vcc, 32, v132
	v_lshl_add_u64 v[0:1], s[0:1], 0, v[2:3]
	s_and_saveexec_b64 s[0:1], vcc
	s_cbranch_execz .LBB1_6
	s_waitcnt lgkmcnt(0)
	v_add_f32_e32 v2, v134, v4
	global_store_dword v[0:1], v2, off

	.amdhsa_kernel _Z6k_mainPKDF16_PKfS2_S2_PKmPjPfS6_
		.amdhsa_group_segment_fixed_size 114688
		.amdhsa_private_segment_fixed_size 0
		.amdhsa_kernarg_size 64
		.amdhsa_user_sgpr_count 2
		.amdhsa_user_sgpr_dispatch_ptr 0
		.amdhsa_user_sgpr_queue_ptr 0
		.amdhsa_user_sgpr_kernarg_segment_ptr 1
		.amdhsa_user_sgpr_dispatch_id 0
		.amdhsa_user_sgpr_kernarg_preload_length 0
		.amdhsa_user_sgpr_kernarg_preload_offset 0
		.amdhsa_user_sgpr_private_segment_size 0
		.amdhsa_uses_dynamic_stack 0
		.amdhsa_enable_private_segment 0
		.amdhsa_system_sgpr_workgroup_id_x 1
		.amdhsa_system_sgpr_workgroup_id_y 0
		.amdhsa_system_sgpr_workgroup_id_z 0
		.amdhsa_system_sgpr_workgroup_info 0
		.amdhsa_system_vgpr_workitem_id 0
		.amdhsa_next_free_vgpr 492
		.amdhsa_next_free_sgpr 102
		.amdhsa_accum_offset 236
		.amdhsa_reserve_vcc 1
		.amdhsa_float_round_mode_32 0
		.amdhsa_float_round_mode_16_64 0
		.amdhsa_float_denorm_mode_32 3
		.amdhsa_float_denorm_mode_16_64 3
		.amdhsa_dx10_clamp 1
		.amdhsa_ieee_mode 1
		.amdhsa_fp16_overflow 0
		.amdhsa_tg_split 0
		.amdhsa_exception_fp_ieee_invalid_op 0
		.amdhsa_exception_fp_denorm_src 0
		.amdhsa_exception_fp_ieee_div_zero 0
		.amdhsa_exception_fp_ieee_overflow 0
		.amdhsa_exception_fp_ieee_underflow 0
		.amdhsa_exception_fp_ieee_inexact 0
		.amdhsa_exception_int_div_zero 0
	.end_amdhsa_kernel

amdhsa.kernels:
  - .agpr_count:     0
    .args:
      - .actual_access:  read_only
        .address_space:  global
        .offset:         0
        .size:           8
        .value_kind:     global_buffer
      - .address_space:  global
        .offset:         8
        .size:           8
        .value_kind:     global_buffer
      - .actual_access:  read_only
        .address_space:  global
        .offset:         16
        .size:           8
        .value_kind:     global_buffer
      - .actual_access:  read_only
        .address_space:  global
        .offset:         24
        .size:           8
        .value_kind:     global_buffer
      - .actual_access:  read_only
        .address_space:  global
        .offset:         32
        .size:           8
        .value_kind:     global_buffer
      - .actual_access:  read_only
        .address_space:  global
        .offset:         40
        .size:           8
        .value_kind:     global_buffer
      - .actual_access:  read_only
        .address_space:  global
        .offset:         48
        .size:           8
        .value_kind:     global_buffer
      - .actual_access:  read_only
        .address_space:  global
        .offset:         56
        .size:           8
        .value_kind:     global_buffer
      - .actual_access:  write_only
        .address_space:  global
        .offset:         64
        .size:           8
        .value_kind:     global_buffer
      - .actual_access:  write_only
        .address_space:  global
        .offset:         72
        .size:           8
        .value_kind:     global_buffer
      - .actual_access:  write_only
        .address_space:  global
        .offset:         80
        .size:           8
        .value_kind:     global_buffer
      - .actual_access:  write_only
        .address_space:  global
        .offset:         88
        .size:           8
        .value_kind:     global_buffer
      - .actual_access:  read_only
        .address_space:  global
        .offset:         96
        .size:           8
        .value_kind:     global_buffer
      - .actual_access:  write_only
        .address_space:  global
        .offset:         104
        .size:           8
        .value_kind:     global_buffer
      - .actual_access:  read_only
        .address_space:  global
        .offset:         112
        .size:           8
        .value_kind:     global_buffer
      - .actual_access:  write_only
        .address_space:  global
        .offset:         120
        .size:           8
        .value_kind:     global_buffer
      - .actual_access:  write_only
        .address_space:  global
        .offset:         128
        .size:           8
        .value_kind:     global_buffer
      - .actual_access:  write_only
        .address_space:  global
        .offset:         136
        .size:           8
        .value_kind:     global_buffer
      - .actual_access:  write_only
        .address_space:  global
        .offset:         144
        .size:           8
        .value_kind:     global_buffer
    .group_segment_fixed_size: 4096
    .kernarg_segment_align: 8
    .kernarg_segment_size: 152
    .language:       OpenCL C
    .language_version:
      - 2
      - 0
    .max_flat_workgroup_size: 512
    .name:           _Z7k_frontPKfPmS0_S0_S0_S0_S0_S0_PDF16_S2_PfS3_S0_S2_S0_S2_S3_S3_S3_
    .private_segment_fixed_size: 0
    .sgpr_count:     88
    .sgpr_spill_count: 0
    .symbol:         _Z7k_frontPKfPmS0_S0_S0_S0_S0_S0_PDF16_S2_PfS3_S0_S2_S0_S2_S3_S3_S3_.kd
    .uniform_work_group_size: 1
    .uses_dynamic_stack: false
    .vgpr_count:     68
    .vgpr_spill_count: 0
    .wavefront_size: 64
  - .agpr_count:     256
    .args:
      - .actual_access:  read_only
        .address_space:  global
        .offset:         0
        .size:           8
        .value_kind:     global_buffer
      - .actual_access:  read_only
        .address_space:  global
        .offset:         8
        .size:           8
        .value_kind:     global_buffer
      - .actual_access:  read_only
        .address_space:  global
        .offset:         16
        .size:           8
        .value_kind:     global_buffer
      - .actual_access:  read_only
        .address_space:  global
        .offset:         24
        .size:           8
        .value_kind:     global_buffer
      - .actual_access:  read_only
        .address_space:  global
        .offset:         32
        .size:           8
        .value_kind:     global_buffer
      - .address_space:  global
        .offset:         40
        .size:           8
        .value_kind:     global_buffer
      - .actual_access:  write_only
        .address_space:  global
        .offset:         48
        .size:           8
        .value_kind:     global_buffer
      - .actual_access:  write_only
        .address_space:  global
        .offset:         56
        .size:           8
        .value_kind:     global_buffer
    .group_segment_fixed_size: 114688
    .kernarg_segment_align: 8
    .kernarg_segment_size: 64
    .language:       OpenCL C
    .language_version:
      - 2
      - 0
    .max_flat_workgroup_size: 256
    .name:           _Z6k_mainPKDF16_PKfS2_S2_PKmPjPfS6_
    .private_segment_fixed_size: 0
    .sgpr_count:     108
    .sgpr_spill_count: 0
    .symbol:         _Z6k_mainPKDF16_PKfS2_S2_PKmPjPfS6_.kd
    .uniform_work_group_size: 1
    .uses_dynamic_stack: false
    .vgpr_count:     492
    .vgpr_spill_count: 0
    .wavefront_size: 64
  - .agpr_count:     0
    .args:
      - .actual_access:  read_only
        .address_space:  global
        .offset:         0
        .size:           8
        .value_kind:     global_buffer
      - .actual_access:  read_only
        .address_space:  global
        .offset:         8
        .size:           8
        .value_kind:     global_buffer
      - .actual_access:  read_only
        .address_space:  global
        .offset:         16
        .size:           8
        .value_kind:     global_buffer
      - .actual_access:  read_only
        .address_space:  global
        .offset:         24
        .size:           8
        .value_kind:     global_buffer
      - .actual_access:  read_only
        .address_space:  global
        .offset:         32
        .size:           8
        .value_kind:     global_buffer
      - .actual_access:  read_only
        .address_space:  global
        .offset:         40
        .size:           8
        .value_kind:     global_buffer
      - .actual_access:  read_only
        .address_space:  global
        .offset:         48
        .size:           8
        .value_kind:     global_buffer
      - .actual_access:  read_only
        .address_space:  global
        .offset:         56
        .size:           8
        .value_kind:     global_buffer
      - .actual_access:  read_only
        .address_space:  global
        .offset:         64
        .size:           8
        .value_kind:     global_buffer
      - .actual_access:  write_only
        .address_space:  global
        .offset:         72
        .size:           8
        .value_kind:     global_buffer
      - .actual_access:  write_only
        .address_space:  global
        .offset:         80
        .size:           8
        .value_kind:     global_buffer
    .group_segment_fixed_size: 101632
    .kernarg_segment_align: 8
    .kernarg_segment_size: 88
    .language:       OpenCL C
    .language_version:
      - 2
      - 0
    .max_flat_workgroup_size: 256
    .name:           _Z7k_graphPKfS0_S0_S0_S0_S0_S0_S0_S0_PfS1_
    .private_segment_fixed_size: 0
    .sgpr_count:     25
    .sgpr_spill_count: 0
    .symbol:         _Z7k_graphPKfS0_S0_S0_S0_S0_S0_S0_S0_PfS1_.kd
    .uniform_work_group_size: 1
    .uses_dynamic_stack: false
    .vgpr_count:     118
    .vgpr_spill_count: 0
    .wavefront_size: 64
  - .agpr_count:     0
    .args:
      - .actual_access:  read_only
        .address_space:  global
        .offset:         0
        .size:           8
        .value_kind:     global_buffer
      - .actual_access:  read_only
        .address_space:  global
        .offset:         8
        .size:           8
        .value_kind:     global_buffer
      - .actual_access:  read_only
        .address_space:  global
        .offset:         16
        .size:           8
        .value_kind:     global_buffer
      - .actual_access:  read_only
        .address_space:  global
        .offset:         24
        .size:           8
        .value_kind:     global_buffer
      - .actual_access:  read_only
        .address_space:  global
        .offset:         32
        .size:           8
        .value_kind:     global_buffer
      - .actual_access:  read_only
        .address_space:  global
        .offset:         40
        .size:           8
        .value_kind:     global_buffer
      - .actual_access:  read_only
        .address_space:  global
        .offset:         48
        .size:           8
        .value_kind:     global_buffer
      - .address_space:  global
        .offset:         56
        .size:           8
        .value_kind:     global_buffer
      - .actual_access:  read_only
        .address_space:  global
        .offset:         64
        .size:           8
        .value_kind:     global_buffer
      - .actual_access:  read_only
        .address_space:  global
        .offset:         72
        .size:           8
        .value_kind:     global_buffer
      - .actual_access:  read_only
        .address_space:  global
        .offset:         80
        .size:           8
        .value_kind:     global_buffer
      - .address_space:  global
        .offset:         88
        .size:           8
        .value_kind:     global_buffer
      - .actual_access:  write_only
        .address_space:  global
        .offset:         96
        .size:           8
        .value_kind:     global_buffer
      - .actual_access:  write_only
        .address_space:  global
        .offset:         104
        .size:           8
        .value_kind:     global_buffer
      - .actual_access:  write_only
        .address_space:  global
        .offset:         112
        .size:           8
        .value_kind:     global_buffer
      - .actual_access:  read_only
        .address_space:  global
        .offset:         120
        .size:           8
        .value_kind:     global_buffer
      - .actual_access:  read_only
        .address_space:  global
        .offset:         128
        .size:           8
        .value_kind:     global_buffer
      - .actual_access:  read_only
        .address_space:  global
        .offset:         136
        .size:           8
        .value_kind:     global_buffer
      - .actual_access:  read_only
        .address_space:  global
        .offset:         144
        .size:           8
        .value_kind:     global_buffer
      - .actual_access:  read_only
        .address_space:  global
        .offset:         152
        .size:           8
        .value_kind:     global_buffer
      - .actual_access:  read_only
        .address_space:  global
        .offset:         160
        .size:           8
        .value_kind:     global_buffer
      - .actual_access:  read_only
        .address_space:  global
        .offset:         168
        .size:           8
        .value_kind:     global_buffer
    .group_segment_fixed_size: 53792
    .kernarg_segment_align: 8
    .kernarg_segment_size: 176
    .language:       OpenCL C
    .language_version:
      - 2
      - 0
    .max_flat_workgroup_size: 512
    .name:           _Z9k_redprepILi1EEvPKfPKjS1_S1_S1_S1_S1_PfPKDv8_DF16_S7_S1_PDF16_S4_S4_S4_PKiS7_S1_S1_S1_S4_S4_
    .private_segment_fixed_size: 0
    .sgpr_count:     106
    .sgpr_spill_count: 4
    .symbol:         _Z9k_redprepILi1EEvPKfPKjS1_S1_S1_S1_S1_PfPKDv8_DF16_S7_S1_PDF16_S4_S4_S4_PKiS7_S1_S1_S1_S4_S4_.kd
    .uniform_work_group_size: 1
    .uses_dynamic_stack: false
    .vgpr_count:     103
    .vgpr_spill_count: 0
    .wavefront_size: 64
  - .agpr_count:     0
    .args:
      - .actual_access:  read_only
        .address_space:  global
        .offset:         0
        .size:           8
        .value_kind:     global_buffer
      - .actual_access:  read_only
        .address_space:  global
        .offset:         8
        .size:           8
        .value_kind:     global_buffer
      - .actual_access:  read_only
        .address_space:  global
        .offset:         16
        .size:           8
        .value_kind:     global_buffer
      - .actual_access:  read_only
        .address_space:  global
        .offset:         24
        .size:           8
        .value_kind:     global_buffer
      - .actual_access:  read_only
        .address_space:  global
        .offset:         32
        .size:           8
        .value_kind:     global_buffer
      - .actual_access:  read_only
        .address_space:  global
        .offset:         40
        .size:           8
        .value_kind:     global_buffer
      - .actual_access:  read_only
        .address_space:  global
        .offset:         48
        .size:           8
        .value_kind:     global_buffer
      - .address_space:  global
        .offset:         56
        .size:           8
        .value_kind:     global_buffer
      - .actual_access:  read_only
        .address_space:  global
        .offset:         64
        .size:           8
        .value_kind:     global_buffer
      - .actual_access:  read_only
        .address_space:  global
        .offset:         72
        .size:           8
        .value_kind:     global_buffer
      - .actual_access:  read_only
        .address_space:  global
        .offset:         80
        .size:           8
        .value_kind:     global_buffer
      - .actual_access:  read_only
        .address_space:  global
        .offset:         88
        .size:           8
        .value_kind:     global_buffer
      - .actual_access:  read_only
        .address_space:  global
        .offset:         96
        .size:           8
        .value_kind:     global_buffer
      - .actual_access:  read_only
        .address_space:  global
        .offset:         104
        .size:           8
        .value_kind:     global_buffer
      - .actual_access:  read_only
        .address_space:  global
        .offset:         112
        .size:           8
        .value_kind:     global_buffer
      - .actual_access:  read_only
        .address_space:  global
        .offset:         120
        .size:           8
        .value_kind:     global_buffer
      - .actual_access:  read_only
        .address_space:  global
        .offset:         128
        .size:           8
        .value_kind:     global_buffer
      - .actual_access:  read_only
        .address_space:  global
        .offset:         136
        .size:           8
        .value_kind:     global_buffer
      - .actual_access:  read_only
        .address_space:  global
        .offset:         144
        .size:           8
        .value_kind:     global_buffer
      - .actual_access:  read_only
        .address_space:  global
        .offset:         152
        .size:           8
        .value_kind:     global_buffer
      - .actual_access:  write_only
        .address_space:  global
        .offset:         160
        .size:           8
        .value_kind:     global_buffer
      - .address_space:  global
        .offset:         168
        .size:           8
        .value_kind:     global_buffer
    .group_segment_fixed_size: 66688
    .kernarg_segment_align: 8
    .kernarg_segment_size: 176
    .language:       OpenCL C
    .language_version:
      - 2
      - 0
    .max_flat_workgroup_size: 512
    .name:           _Z9k_redprepILi2EEvPKfPKjS1_S1_S1_S1_S1_PfPKDv8_DF16_S7_S1_PDF16_S4_S4_S4_PKiS7_S1_S1_S1_S4_S4_
    .private_segment_fixed_size: 0
    .sgpr_count:     102
    .sgpr_spill_count: 0
    .symbol:         _Z9k_redprepILi2EEvPKfPKjS1_S1_S1_S1_S1_PfPKDv8_DF16_S7_S1_PDF16_S4_S4_S4_PKiS7_S1_S1_S1_S4_S4_.kd
    .uniform_work_group_size: 1
    .uses_dynamic_stack: false
    .vgpr_count:     106
    .vgpr_spill_count: 0
    .wavefront_size: 64
